# adds: moe2 gate loads hoisted out of the epilogue, scatter expert-count scan loads batched, combine+norm row loads batched per token
# speedup vs baseline: 1.0283x; 1.0048x over previous
.LBB0_940:
	s_or_b64 exec, exec, s[64:65]
	s_mov_b32 s0, s37
	s_waitcnt lgkmcnt(0)
	s_barrier
	s_mov_b32 s1, s33
	v_mbcnt_lo_u32_b32 v0, -1, s0
	v_mbcnt_hi_u32_b32 v0, -1, v0
	v_lshl_or_b32 v2, s1, 6, v0
	v_readlane_b32 s0, v254, 0
	s_mov_b32 s17, s0
	s_mov_b32 s0, s37
	s_add_i32 s0, s0, 0x20120
	v_mov_b32_e32 v0, s0
	ds_read_b64 v[0:1], v0
	s_mov_b32 s0, 0
	s_add_i32 s0, s0, 0x20120
	s_mov_b32 s4, s60
	s_waitcnt lgkmcnt(0)
	v_readfirstlane_b32 s16, v0
	v_mov_b32_e32 v0, s0
	v_readfirstlane_b32 s14, v1
	ds_read_b64 v[0:1], v0
	s_mov_b32 s0, 0
	s_add_i32 s0, s0, 0x20120
	v_readlane_b32 s1, v254, 1
	s_waitcnt lgkmcnt(0)
	v_readfirstlane_b32 s12, v0
	v_mov_b32_e32 v0, s0
	v_readfirstlane_b32 s5, v1
	ds_read_b64 v[0:1], v0
	s_mov_b32 s0, 0
	s_add_i32 s0, s0, 0x20120
	s_waitcnt lgkmcnt(0)
	v_readfirstlane_b32 s8, v0
	v_mov_b32_e32 v0, s0
	v_readfirstlane_b32 s2, v1
	ds_read_b64 v[0:1], v0
	s_mov_b32 s0, 0
	s_add_i32 s0, s0, 0x20120
	s_waitcnt lgkmcnt(0)
	v_readfirstlane_b32 s23, v0
	v_mov_b32_e32 v0, s0
	v_readfirstlane_b32 s22, v1
	ds_read_b64 v[0:1], v0
	s_mov_b32 s0, 0
	s_add_i32 s0, s0, 0x20120
	s_waitcnt lgkmcnt(0)
	v_readfirstlane_b32 s15, v0
	v_mov_b32_e32 v0, s0
	v_readfirstlane_b32 s13, v1
	ds_read_b64 v[0:1], v0
	s_mov_b32 s0, 0
	s_add_i32 s0, s0, 0x200b8
	s_waitcnt lgkmcnt(0)
	v_readfirstlane_b32 s19, v0
	v_mov_b32_e32 v0, s0
	v_readfirstlane_b32 s18, v1
	ds_read_b64 v[0:1], v0
	s_mov_b32 s0, 0
	s_add_i32 s0, s0, 0x20120
	s_waitcnt lgkmcnt(0)
	v_readfirstlane_b32 s25, v0
	v_mov_b32_e32 v0, s0
	v_readfirstlane_b32 s24, v1
	ds_read_b64 v[0:1], v0
	s_mov_b32 s0, 0
	s_add_i32 s0, s0, 0x20120
	s_waitcnt lgkmcnt(0)
	v_readfirstlane_b32 s21, v0
	v_mov_b32_e32 v0, s0
	v_readfirstlane_b32 s20, v1
	ds_read_b64 v[0:1], v0
	s_mov_b32 s0, 0
	s_add_i32 s0, s0, 0x20120
	s_waitcnt lgkmcnt(0)
	v_readfirstlane_b32 s27, v0
	v_mov_b32_e32 v0, s0
	v_readfirstlane_b32 s26, v1
	ds_read_b64 v[0:1], v0
	v_cmp_eq_u32_e64 s[0:1], 0, v2
	s_waitcnt lgkmcnt(0)
	v_readfirstlane_b32 s28, v1
	v_readfirstlane_b32 s29, v0
	s_and_saveexec_b64 s[6:7], s[0:1]
	s_cbranch_execz .LBB0_942
	v_readlane_b32 s9, v254, 9
	v_mov_b32_e32 v1, s2
	s_nop 0
	v_mov_b32_e32 v0, s9
	ds_write_b32 v0, v145
	v_mov_b32_e32 v0, s8
	v_add_co_u32_e32 v0, vcc, 0x1e76b000, v0
	s_add_u32 s8, s8, 0x1e76b600
	s_nop 0
	v_addc_co_u32_e32 v1, vcc, 0, v1, vcc
	global_load_dwordx4 v[68:71], v[0:1], off offset:1536
	global_load_dwordx4 v[72:75], v[0:1], off offset:1552
	global_load_dwordx4 v[76:79], v[0:1], off offset:1568
	global_load_dwordx4 v[80:83], v[0:1], off offset:1584
	global_load_dwordx4 v[84:87], v[0:1], off offset:1600
	global_load_dwordx4 v[88:91], v[0:1], off offset:1616
	global_load_dwordx4 v[92:95], v[0:1], off offset:1632
	global_load_dwordx4 v[96:99], v[0:1], off offset:1648
	global_load_dwordx4 v[100:103], v[0:1], off offset:1664
	global_load_dwordx4 v[104:107], v[0:1], off offset:1680
	global_load_dwordx4 v[108:111], v[0:1], off offset:1696
	global_load_dwordx4 v[112:115], v[0:1], off offset:1712
	global_load_dwordx4 v[116:119], v[0:1], off offset:1728
	global_load_dwordx4 v[120:123], v[0:1], off offset:1744
	global_load_dwordx4 v[124:127], v[0:1], off offset:1760
	global_load_dwordx4 v[128:131], v[0:1], off offset:1776
	s_waitcnt vmcnt(0)
	v_mov_b32_e32 v3, v68
	v_readlane_b32 s9, v254, 10
	s_nop 0
	v_add_u32_e32 v3, 0x13f, v3
	v_mov_b32_e32 v4, s9
	s_addc_u32 s9, s2, 0
	v_mov_b64_e32 v[0:1], s[8:9]
	s_mov_b32 s8, 0x66666667
	v_mul_hi_i32 v3, v3, s8
	v_lshrrev_b32_e32 v5, 31, v3
	v_ashrrev_i32_e32 v3, 7, v3
	v_add_u32_e32 v3, v3, v5
	s_movk_i32 s2, 0x140
	v_mul_lo_u32 v3, v3, s2
	ds_write_b32 v4, v3
	v_mov_b32_e32 v4, v69
	v_readlane_b32 s9, v254, 11
	s_nop 0
	v_add_u32_e32 v4, 0x13f, v4
	v_mul_hi_i32 v6, v4, s8
	v_lshrrev_b32_e32 v7, 31, v6
	v_ashrrev_i32_e32 v6, 7, v6
	v_add_u32_e32 v6, v6, v7
	v_mul_lo_u32 v6, v6, s2
	v_sub_u32_e32 v6, v6, v4
	v_mov_b32_e32 v5, s9
	v_add3_u32 v3, v4, v3, v6
	ds_write_b32 v5, v3
	v_mov_b32_e32 v4, v70
	v_readlane_b32 s9, v254, 12
	s_nop 0
	v_add_u32_e32 v4, 0x13f, v4
	v_mul_hi_i32 v6, v4, s8
	v_lshrrev_b32_e32 v7, 31, v6
	v_ashrrev_i32_e32 v6, 7, v6
	v_add_u32_e32 v6, v6, v7
	v_mul_lo_u32 v6, v6, s2
	v_sub_u32_e32 v6, v6, v4
	v_mov_b32_e32 v5, s9
	v_add3_u32 v3, v4, v3, v6
	ds_write_b32 v5, v3
	v_mov_b32_e32 v4, v71
	v_readlane_b32 s9, v254, 13
	s_nop 0
	v_add_u32_e32 v4, 0x13f, v4
	v_mul_hi_i32 v6, v4, s8
	v_lshrrev_b32_e32 v7, 31, v6
	v_ashrrev_i32_e32 v6, 7, v6
	v_add_u32_e32 v6, v6, v7
	v_mul_lo_u32 v6, v6, s2
	v_sub_u32_e32 v6, v6, v4
	v_mov_b32_e32 v5, s9
	v_add3_u32 v3, v4, v3, v6
	ds_write_b32 v5, v3
	v_mov_b32_e32 v4, v72
	v_readlane_b32 s9, v254, 14
	s_nop 0
	v_add_u32_e32 v4, 0x13f, v4
	v_mul_hi_i32 v6, v4, s8
	v_lshrrev_b32_e32 v7, 31, v6
	v_ashrrev_i32_e32 v6, 7, v6
	v_add_u32_e32 v6, v6, v7
	v_mul_lo_u32 v6, v6, s2
	v_sub_u32_e32 v6, v6, v4
	v_mov_b32_e32 v5, s9
	v_add3_u32 v3, v4, v3, v6
	ds_write_b32 v5, v3
	v_mov_b32_e32 v4, v73
	v_readlane_b32 s9, v254, 15
	s_nop 0
	v_add_u32_e32 v4, 0x13f, v4
	v_mul_hi_i32 v6, v4, s8
	v_lshrrev_b32_e32 v7, 31, v6
	v_ashrrev_i32_e32 v6, 7, v6
	v_add_u32_e32 v6, v6, v7
	v_mul_lo_u32 v6, v6, s2
	v_sub_u32_e32 v6, v6, v4
	v_mov_b32_e32 v5, s9
	v_add3_u32 v3, v4, v3, v6
	ds_write_b32 v5, v3
	v_mov_b32_e32 v4, v74
	v_readlane_b32 s9, v254, 16
	s_nop 0
	v_add_u32_e32 v4, 0x13f, v4
	v_mul_hi_i32 v6, v4, s8
	v_lshrrev_b32_e32 v7, 31, v6
	v_ashrrev_i32_e32 v6, 7, v6
	v_add_u32_e32 v6, v6, v7
	v_mul_lo_u32 v6, v6, s2
	v_sub_u32_e32 v6, v6, v4
	v_mov_b32_e32 v5, s9
	v_add3_u32 v3, v4, v3, v6
	ds_write_b32 v5, v3
	v_mov_b32_e32 v4, v75
	v_readlane_b32 s9, v254, 17
	s_nop 0
	v_add_u32_e32 v4, 0x13f, v4
	v_mul_hi_i32 v6, v4, s8
	v_lshrrev_b32_e32 v7, 31, v6
	v_ashrrev_i32_e32 v6, 7, v6
	v_add_u32_e32 v6, v6, v7
	v_mul_lo_u32 v6, v6, s2
	v_sub_u32_e32 v6, v6, v4
	v_mov_b32_e32 v5, s9
	v_add3_u32 v3, v4, v3, v6
	ds_write_b32 v5, v3
	v_mov_b32_e32 v4, v76
	v_readlane_b32 s9, v254, 18
	s_nop 0
	v_add_u32_e32 v4, 0x13f, v4
	v_mul_hi_i32 v6, v4, s8
	v_lshrrev_b32_e32 v7, 31, v6
	v_ashrrev_i32_e32 v6, 7, v6
	v_add_u32_e32 v6, v6, v7
	v_mul_lo_u32 v6, v6, s2
	v_sub_u32_e32 v6, v6, v4
	v_mov_b32_e32 v5, s9
	v_add3_u32 v3, v4, v3, v6
	ds_write_b32 v5, v3
	v_mov_b32_e32 v4, v77
	v_readlane_b32 s9, v254, 19
	s_nop 0
	v_add_u32_e32 v4, 0x13f, v4
	v_mul_hi_i32 v6, v4, s8
	v_lshrrev_b32_e32 v7, 31, v6
	v_ashrrev_i32_e32 v6, 7, v6
	v_add_u32_e32 v6, v6, v7
	v_mul_lo_u32 v6, v6, s2
	v_sub_u32_e32 v6, v6, v4
	v_mov_b32_e32 v5, s9
	v_add3_u32 v3, v4, v3, v6
	ds_write_b32 v5, v3
	v_mov_b32_e32 v4, v78
	v_readlane_b32 s9, v254, 20
	s_nop 0
	v_add_u32_e32 v4, 0x13f, v4
	v_mul_hi_i32 v6, v4, s8
	v_lshrrev_b32_e32 v7, 31, v6
	v_ashrrev_i32_e32 v6, 7, v6
	v_add_u32_e32 v6, v6, v7
	v_mul_lo_u32 v6, v6, s2
	v_sub_u32_e32 v6, v6, v4
	v_mov_b32_e32 v5, s9
	v_add3_u32 v3, v4, v3, v6
	ds_write_b32 v5, v3
	v_mov_b32_e32 v4, v79
	v_readlane_b32 s9, v254, 21
	s_nop 0
	v_add_u32_e32 v4, 0x13f, v4
	v_mul_hi_i32 v6, v4, s8
	v_lshrrev_b32_e32 v7, 31, v6
	v_ashrrev_i32_e32 v6, 7, v6
	v_add_u32_e32 v6, v6, v7
	v_mul_lo_u32 v6, v6, s2
	v_sub_u32_e32 v6, v6, v4
	v_mov_b32_e32 v5, s9
	v_add3_u32 v3, v4, v3, v6
	ds_write_b32 v5, v3
	v_mov_b32_e32 v4, v80
	v_readlane_b32 s9, v254, 22
	s_nop 0
	v_add_u32_e32 v4, 0x13f, v4
	v_mul_hi_i32 v6, v4, s8
	v_lshrrev_b32_e32 v7, 31, v6
	v_ashrrev_i32_e32 v6, 7, v6
	v_add_u32_e32 v6, v6, v7
	v_mul_lo_u32 v6, v6, s2
	v_sub_u32_e32 v6, v6, v4
	v_mov_b32_e32 v5, s9
	v_add3_u32 v3, v4, v3, v6
	ds_write_b32 v5, v3
	v_mov_b32_e32 v4, v81
	v_readlane_b32 s9, v254, 23
	s_nop 0
	v_add_u32_e32 v4, 0x13f, v4
	v_mul_hi_i32 v6, v4, s8
	v_lshrrev_b32_e32 v7, 31, v6
	v_ashrrev_i32_e32 v6, 7, v6
	v_add_u32_e32 v6, v6, v7
	v_mul_lo_u32 v6, v6, s2
	v_sub_u32_e32 v6, v6, v4
	v_mov_b32_e32 v5, s9
	v_add3_u32 v3, v4, v3, v6
	ds_write_b32 v5, v3
	v_mov_b32_e32 v4, v82
	v_readlane_b32 s9, v254, 24
	s_nop 0
	v_add_u32_e32 v4, 0x13f, v4
	v_mul_hi_i32 v6, v4, s8
	v_lshrrev_b32_e32 v7, 31, v6
	v_ashrrev_i32_e32 v6, 7, v6
	v_add_u32_e32 v6, v6, v7
	v_mul_lo_u32 v6, v6, s2
	v_sub_u32_e32 v6, v6, v4
	v_mov_b32_e32 v5, s9
	v_add3_u32 v3, v4, v3, v6
	ds_write_b32 v5, v3
	v_mov_b32_e32 v4, v83
	v_readlane_b32 s9, v254, 25
	s_nop 0
	v_add_u32_e32 v4, 0x13f, v4
	v_mul_hi_i32 v6, v4, s8
	v_lshrrev_b32_e32 v7, 31, v6
	v_ashrrev_i32_e32 v6, 7, v6
	v_add_u32_e32 v6, v6, v7
	v_mul_lo_u32 v6, v6, s2
	v_sub_u32_e32 v6, v6, v4
	v_mov_b32_e32 v5, s9
	v_add3_u32 v3, v4, v3, v6
	ds_write_b32 v5, v3
	v_mov_b32_e32 v4, v84
	v_readlane_b32 s9, v254, 26
	s_nop 0
	v_add_u32_e32 v4, 0x13f, v4
	v_mul_hi_i32 v6, v4, s8
	v_lshrrev_b32_e32 v7, 31, v6
	v_ashrrev_i32_e32 v6, 7, v6
	v_add_u32_e32 v6, v6, v7
	v_mul_lo_u32 v6, v6, s2
	v_sub_u32_e32 v6, v6, v4
	v_mov_b32_e32 v5, s9
	v_add3_u32 v3, v4, v3, v6
	ds_write_b32 v5, v3
	v_mov_b32_e32 v4, v85
	v_readlane_b32 s9, v254, 27
	s_nop 0
	v_add_u32_e32 v4, 0x13f, v4
	v_mul_hi_i32 v6, v4, s8
	v_lshrrev_b32_e32 v7, 31, v6
	v_ashrrev_i32_e32 v6, 7, v6
	v_add_u32_e32 v6, v6, v7
	v_mul_lo_u32 v6, v6, s2
	v_sub_u32_e32 v6, v6, v4
	v_mov_b32_e32 v5, s9
	v_add3_u32 v3, v4, v3, v6
	ds_write_b32 v5, v3
	v_mov_b32_e32 v4, v86
	v_readlane_b32 s9, v254, 28
	s_nop 0
	v_add_u32_e32 v4, 0x13f, v4
	v_mul_hi_i32 v6, v4, s8
	v_lshrrev_b32_e32 v7, 31, v6
	v_ashrrev_i32_e32 v6, 7, v6
	v_add_u32_e32 v6, v6, v7
	v_mul_lo_u32 v6, v6, s2
	v_sub_u32_e32 v6, v6, v4
	v_mov_b32_e32 v5, s9
	v_add3_u32 v3, v4, v3, v6
	ds_write_b32 v5, v3
	v_mov_b32_e32 v4, v87
	v_readlane_b32 s9, v254, 29
	s_nop 0
	v_add_u32_e32 v4, 0x13f, v4
	v_mul_hi_i32 v6, v4, s8
	v_lshrrev_b32_e32 v7, 31, v6
	v_ashrrev_i32_e32 v6, 7, v6
	v_add_u32_e32 v6, v6, v7
	v_mul_lo_u32 v6, v6, s2
	v_sub_u32_e32 v6, v6, v4
	v_mov_b32_e32 v5, s9
	v_add3_u32 v3, v4, v3, v6
	ds_write_b32 v5, v3
	v_mov_b32_e32 v4, v88
	v_readlane_b32 s9, v254, 30
	s_nop 0
	v_add_u32_e32 v4, 0x13f, v4
	v_mul_hi_i32 v6, v4, s8
	v_lshrrev_b32_e32 v7, 31, v6
	v_ashrrev_i32_e32 v6, 7, v6
	v_add_u32_e32 v6, v6, v7
	v_mul_lo_u32 v6, v6, s2
	v_sub_u32_e32 v6, v6, v4
	v_mov_b32_e32 v5, s9
	v_add3_u32 v3, v4, v3, v6
	ds_write_b32 v5, v3
	v_mov_b32_e32 v4, v89
	v_readlane_b32 s9, v254, 31
	s_nop 0
	v_add_u32_e32 v4, 0x13f, v4
	v_mul_hi_i32 v6, v4, s8
	v_lshrrev_b32_e32 v7, 31, v6
	v_ashrrev_i32_e32 v6, 7, v6
	v_add_u32_e32 v6, v6, v7
	v_mul_lo_u32 v6, v6, s2
	v_sub_u32_e32 v6, v6, v4
	v_mov_b32_e32 v5, s9
	v_add3_u32 v3, v4, v3, v6
	ds_write_b32 v5, v3
	v_mov_b32_e32 v4, v90
	v_readlane_b32 s9, v254, 32
	s_nop 0
	v_add_u32_e32 v4, 0x13f, v4
	v_mul_hi_i32 v6, v4, s8
	v_lshrrev_b32_e32 v7, 31, v6
	v_ashrrev_i32_e32 v6, 7, v6
	v_add_u32_e32 v6, v6, v7
	v_mul_lo_u32 v6, v6, s2
	v_sub_u32_e32 v6, v6, v4
	v_mov_b32_e32 v5, s9
	v_add3_u32 v3, v4, v3, v6
	ds_write_b32 v5, v3
	v_mov_b32_e32 v4, v91
	v_readlane_b32 s9, v254, 33
	s_nop 0
	v_add_u32_e32 v4, 0x13f, v4
	v_mul_hi_i32 v6, v4, s8
	v_lshrrev_b32_e32 v7, 31, v6
	v_ashrrev_i32_e32 v6, 7, v6
	v_add_u32_e32 v6, v6, v7
	v_mul_lo_u32 v6, v6, s2
	v_sub_u32_e32 v6, v6, v4
	v_mov_b32_e32 v5, s9
	v_add3_u32 v3, v4, v3, v6
	ds_write_b32 v5, v3
	v_mov_b32_e32 v4, v92
	v_readlane_b32 s9, v254, 34
	s_nop 0
	v_add_u32_e32 v4, 0x13f, v4
	v_mul_hi_i32 v6, v4, s8
	v_lshrrev_b32_e32 v7, 31, v6
	v_ashrrev_i32_e32 v6, 7, v6
	v_add_u32_e32 v6, v6, v7
	v_mul_lo_u32 v6, v6, s2
	v_sub_u32_e32 v6, v6, v4
	v_mov_b32_e32 v5, s9
	v_add3_u32 v3, v4, v3, v6
	ds_write_b32 v5, v3
	v_mov_b32_e32 v4, v93
	v_readlane_b32 s9, v254, 35
	s_nop 0
	v_add_u32_e32 v4, 0x13f, v4
	v_mul_hi_i32 v6, v4, s8
	v_lshrrev_b32_e32 v7, 31, v6
	v_ashrrev_i32_e32 v6, 7, v6
	v_add_u32_e32 v6, v6, v7
	v_mul_lo_u32 v6, v6, s2
	v_sub_u32_e32 v6, v6, v4
	v_mov_b32_e32 v5, s9
	v_add3_u32 v3, v4, v3, v6
	ds_write_b32 v5, v3
	v_mov_b32_e32 v4, v94
	v_readlane_b32 s9, v254, 36
	s_nop 0
	v_add_u32_e32 v4, 0x13f, v4
	v_mul_hi_i32 v6, v4, s8
	v_lshrrev_b32_e32 v7, 31, v6
	v_ashrrev_i32_e32 v6, 7, v6
	v_add_u32_e32 v6, v6, v7
	v_mul_lo_u32 v6, v6, s2
	v_sub_u32_e32 v6, v6, v4
	v_mov_b32_e32 v5, s9
	v_add3_u32 v3, v4, v3, v6
	ds_write_b32 v5, v3
	v_mov_b32_e32 v4, v95
	v_readlane_b32 s9, v254, 37
	s_nop 0
	v_add_u32_e32 v4, 0x13f, v4
	v_mul_hi_i32 v6, v4, s8
	v_lshrrev_b32_e32 v7, 31, v6
	v_ashrrev_i32_e32 v6, 7, v6
	v_add_u32_e32 v6, v6, v7
	v_mul_lo_u32 v6, v6, s2
	v_sub_u32_e32 v6, v6, v4
	v_mov_b32_e32 v5, s9
	v_add3_u32 v3, v4, v3, v6
	ds_write_b32 v5, v3
	v_mov_b32_e32 v4, v96
	v_readlane_b32 s9, v254, 38
	s_nop 0
	v_add_u32_e32 v4, 0x13f, v4
	v_mul_hi_i32 v6, v4, s8
	v_lshrrev_b32_e32 v7, 31, v6
	v_ashrrev_i32_e32 v6, 7, v6
	v_add_u32_e32 v6, v6, v7
	v_mul_lo_u32 v6, v6, s2
	v_sub_u32_e32 v6, v6, v4
	v_mov_b32_e32 v5, s9
	v_add3_u32 v3, v4, v3, v6
	ds_write_b32 v5, v3
	v_mov_b32_e32 v4, v97
	v_readlane_b32 s9, v254, 39
	s_nop 0
	v_add_u32_e32 v4, 0x13f, v4
	v_mul_hi_i32 v6, v4, s8
	v_lshrrev_b32_e32 v7, 31, v6
	v_ashrrev_i32_e32 v6, 7, v6
	v_add_u32_e32 v6, v6, v7
	v_mul_lo_u32 v6, v6, s2
	v_sub_u32_e32 v6, v6, v4
	v_mov_b32_e32 v5, s9
	v_add3_u32 v3, v4, v3, v6
	ds_write_b32 v5, v3
	v_mov_b32_e32 v4, v98
	v_readlane_b32 s9, v254, 40
	s_nop 0
	v_add_u32_e32 v4, 0x13f, v4
	v_mul_hi_i32 v6, v4, s8
	v_lshrrev_b32_e32 v7, 31, v6
	v_ashrrev_i32_e32 v6, 7, v6
	v_add_u32_e32 v6, v6, v7
	v_mul_lo_u32 v6, v6, s2
	v_sub_u32_e32 v6, v6, v4
	v_mov_b32_e32 v5, s9
	v_add3_u32 v3, v4, v3, v6
	ds_write_b32 v5, v3
	v_mov_b32_e32 v4, v99
	v_readlane_b32 s9, v254, 41
	s_nop 0
	v_add_u32_e32 v4, 0x13f, v4
	v_mul_hi_i32 v6, v4, s8
	v_lshrrev_b32_e32 v7, 31, v6
	v_ashrrev_i32_e32 v6, 7, v6
	v_add_u32_e32 v6, v6, v7
	v_mul_lo_u32 v6, v6, s2
	v_sub_u32_e32 v6, v6, v4
	v_mov_b32_e32 v5, s9
	v_add3_u32 v3, v4, v3, v6
	ds_write_b32 v5, v3
	v_mov_b32_e32 v4, v100
	v_readlane_b32 s9, v254, 42
	s_nop 0
	v_add_u32_e32 v4, 0x13f, v4
	v_mul_hi_i32 v6, v4, s8
	v_lshrrev_b32_e32 v7, 31, v6
	v_ashrrev_i32_e32 v6, 7, v6
	v_add_u32_e32 v6, v6, v7
	v_mul_lo_u32 v6, v6, s2
	v_sub_u32_e32 v6, v6, v4
	v_mov_b32_e32 v5, s9
	v_add3_u32 v3, v4, v3, v6
	ds_write_b32 v5, v3
	v_mov_b32_e32 v4, v101
	v_readlane_b32 s9, v254, 43
	s_nop 0
	v_add_u32_e32 v4, 0x13f, v4
	v_mul_hi_i32 v6, v4, s8
	v_lshrrev_b32_e32 v7, 31, v6
	v_ashrrev_i32_e32 v6, 7, v6
	v_add_u32_e32 v6, v6, v7
	v_mul_lo_u32 v6, v6, s2
	v_sub_u32_e32 v6, v6, v4
	v_mov_b32_e32 v5, s9
	v_add3_u32 v3, v4, v3, v6
	ds_write_b32 v5, v3
	v_mov_b32_e32 v4, v102
	v_readlane_b32 s9, v254, 44
	s_nop 0
	v_add_u32_e32 v4, 0x13f, v4
	v_mul_hi_i32 v6, v4, s8
	v_lshrrev_b32_e32 v7, 31, v6
	v_ashrrev_i32_e32 v6, 7, v6
	v_add_u32_e32 v6, v6, v7
	v_mul_lo_u32 v6, v6, s2
	v_sub_u32_e32 v6, v6, v4
	v_mov_b32_e32 v5, s9
	v_add3_u32 v3, v4, v3, v6
	ds_write_b32 v5, v3
	v_mov_b32_e32 v4, v103
	v_readlane_b32 s9, v254, 45
	s_nop 0
	v_add_u32_e32 v4, 0x13f, v4
	v_mul_hi_i32 v6, v4, s8
	v_lshrrev_b32_e32 v7, 31, v6
	v_ashrrev_i32_e32 v6, 7, v6
	v_add_u32_e32 v6, v6, v7
	v_mul_lo_u32 v6, v6, s2
	v_sub_u32_e32 v6, v6, v4
	v_mov_b32_e32 v5, s9
	v_add3_u32 v3, v4, v3, v6
	ds_write_b32 v5, v3
	v_mov_b32_e32 v4, v104
	v_readlane_b32 s9, v254, 46
	s_nop 0
	v_add_u32_e32 v4, 0x13f, v4
	v_mul_hi_i32 v6, v4, s8
	v_lshrrev_b32_e32 v7, 31, v6
	v_ashrrev_i32_e32 v6, 7, v6
	v_add_u32_e32 v6, v6, v7
	v_mul_lo_u32 v6, v6, s2
	v_sub_u32_e32 v6, v6, v4
	v_mov_b32_e32 v5, s9
	v_add3_u32 v3, v4, v3, v6
	ds_write_b32 v5, v3
	v_mov_b32_e32 v4, v105
	v_readlane_b32 s9, v254, 47
	s_nop 0
	v_add_u32_e32 v4, 0x13f, v4
	v_mul_hi_i32 v6, v4, s8
	v_lshrrev_b32_e32 v7, 31, v6
	v_ashrrev_i32_e32 v6, 7, v6
	v_add_u32_e32 v6, v6, v7
	v_mul_lo_u32 v6, v6, s2
	v_sub_u32_e32 v6, v6, v4
	v_mov_b32_e32 v5, s9
	v_add3_u32 v3, v4, v3, v6
	ds_write_b32 v5, v3
	v_mov_b32_e32 v4, v106
	v_readlane_b32 s9, v254, 48
	s_nop 0
	v_add_u32_e32 v4, 0x13f, v4
	v_mul_hi_i32 v6, v4, s8
	v_lshrrev_b32_e32 v7, 31, v6
	v_ashrrev_i32_e32 v6, 7, v6
	v_add_u32_e32 v6, v6, v7
	v_mul_lo_u32 v6, v6, s2
	v_sub_u32_e32 v6, v6, v4
	v_mov_b32_e32 v5, s9
	v_add3_u32 v3, v4, v3, v6
	ds_write_b32 v5, v3
	v_mov_b32_e32 v4, v107
	v_readlane_b32 s9, v254, 49
	s_nop 0
	v_add_u32_e32 v4, 0x13f, v4
	v_mul_hi_i32 v6, v4, s8
	v_lshrrev_b32_e32 v7, 31, v6
	v_ashrrev_i32_e32 v6, 7, v6
	v_add_u32_e32 v6, v6, v7
	v_mul_lo_u32 v6, v6, s2
	v_sub_u32_e32 v6, v6, v4
	v_mov_b32_e32 v5, s9
	v_add3_u32 v3, v4, v3, v6
	ds_write_b32 v5, v3
	v_mov_b32_e32 v4, v108
	v_readlane_b32 s9, v254, 50
	s_nop 0
	v_add_u32_e32 v4, 0x13f, v4
	v_mul_hi_i32 v6, v4, s8
	v_lshrrev_b32_e32 v7, 31, v6
	v_ashrrev_i32_e32 v6, 7, v6
	v_add_u32_e32 v6, v6, v7
	v_mul_lo_u32 v6, v6, s2
	v_sub_u32_e32 v6, v6, v4
	v_mov_b32_e32 v5, s9
	v_add3_u32 v3, v4, v3, v6
	ds_write_b32 v5, v3
	v_mov_b32_e32 v4, v109
	v_readlane_b32 s9, v254, 51
	s_nop 0
	v_add_u32_e32 v4, 0x13f, v4
	v_mul_hi_i32 v6, v4, s8
	v_lshrrev_b32_e32 v7, 31, v6
	v_ashrrev_i32_e32 v6, 7, v6
	v_add_u32_e32 v6, v6, v7
	v_mul_lo_u32 v6, v6, s2
	v_sub_u32_e32 v6, v6, v4
	v_mov_b32_e32 v5, s9
	v_add3_u32 v3, v4, v3, v6
	ds_write_b32 v5, v3
	v_mov_b32_e32 v4, v110
	v_readlane_b32 s9, v254, 52
	s_nop 0
	v_add_u32_e32 v4, 0x13f, v4
	v_mul_hi_i32 v6, v4, s8
	v_lshrrev_b32_e32 v7, 31, v6
	v_ashrrev_i32_e32 v6, 7, v6
	v_add_u32_e32 v6, v6, v7
	v_mul_lo_u32 v6, v6, s2
	v_sub_u32_e32 v6, v6, v4
	v_mov_b32_e32 v5, s9
	v_add3_u32 v3, v4, v3, v6
	ds_write_b32 v5, v3
	v_mov_b32_e32 v4, v111
	v_readlane_b32 s9, v254, 53
	s_nop 0
	v_add_u32_e32 v4, 0x13f, v4
	v_mul_hi_i32 v6, v4, s8
	v_lshrrev_b32_e32 v7, 31, v6
	v_ashrrev_i32_e32 v6, 7, v6
	v_add_u32_e32 v6, v6, v7
	v_mul_lo_u32 v6, v6, s2
	v_sub_u32_e32 v6, v6, v4
	v_mov_b32_e32 v5, s9
	v_add3_u32 v3, v4, v3, v6
	ds_write_b32 v5, v3
	v_mov_b32_e32 v4, v112
	v_readlane_b32 s9, v254, 54
	s_nop 0
	v_add_u32_e32 v4, 0x13f, v4
	v_mul_hi_i32 v6, v4, s8
	v_lshrrev_b32_e32 v7, 31, v6
	v_ashrrev_i32_e32 v6, 7, v6
	v_add_u32_e32 v6, v6, v7
	v_mul_lo_u32 v6, v6, s2
	v_sub_u32_e32 v6, v6, v4
	v_mov_b32_e32 v5, s9
	v_add3_u32 v3, v4, v3, v6
	ds_write_b32 v5, v3
	v_mov_b32_e32 v4, v113
	v_readlane_b32 s9, v254, 55
	s_nop 0
	v_add_u32_e32 v4, 0x13f, v4
	v_mul_hi_i32 v6, v4, s8
	v_lshrrev_b32_e32 v7, 31, v6
	v_ashrrev_i32_e32 v6, 7, v6
	v_add_u32_e32 v6, v6, v7
	v_mul_lo_u32 v6, v6, s2
	v_sub_u32_e32 v6, v6, v4
	v_mov_b32_e32 v5, s9
	v_add3_u32 v3, v4, v3, v6
	ds_write_b32 v5, v3
	v_mov_b32_e32 v4, v114
	v_readlane_b32 s9, v254, 56
	s_nop 0
	v_add_u32_e32 v4, 0x13f, v4
	v_mul_hi_i32 v6, v4, s8
	v_lshrrev_b32_e32 v7, 31, v6
	v_ashrrev_i32_e32 v6, 7, v6
	v_add_u32_e32 v6, v6, v7
	v_mul_lo_u32 v6, v6, s2
	v_sub_u32_e32 v6, v6, v4
	v_mov_b32_e32 v5, s9
	v_add3_u32 v3, v4, v3, v6
	ds_write_b32 v5, v3
	v_mov_b32_e32 v4, v115
	v_readlane_b32 s9, v254, 57
	s_nop 0
	v_add_u32_e32 v4, 0x13f, v4
	v_mul_hi_i32 v6, v4, s8
	v_lshrrev_b32_e32 v7, 31, v6
	v_ashrrev_i32_e32 v6, 7, v6
	v_add_u32_e32 v6, v6, v7
	v_mul_lo_u32 v6, v6, s2
	v_sub_u32_e32 v6, v6, v4
	v_mov_b32_e32 v5, s9
	v_add3_u32 v3, v4, v3, v6
	ds_write_b32 v5, v3
	v_mov_b32_e32 v4, v116
	v_readlane_b32 s9, v254, 58
	s_nop 0
	v_add_u32_e32 v4, 0x13f, v4
	v_mul_hi_i32 v6, v4, s8
	v_lshrrev_b32_e32 v7, 31, v6
	v_ashrrev_i32_e32 v6, 7, v6
	v_add_u32_e32 v6, v6, v7
	v_mul_lo_u32 v6, v6, s2
	v_sub_u32_e32 v6, v6, v4
	v_mov_b32_e32 v5, s9
	v_add3_u32 v3, v4, v3, v6
	ds_write_b32 v5, v3
	v_mov_b32_e32 v4, v117
	v_readlane_b32 s9, v254, 59
	s_nop 0
	v_add_u32_e32 v4, 0x13f, v4
	v_mul_hi_i32 v6, v4, s8
	v_lshrrev_b32_e32 v7, 31, v6
	v_ashrrev_i32_e32 v6, 7, v6
	v_add_u32_e32 v6, v6, v7
	v_mul_lo_u32 v6, v6, s2
	v_sub_u32_e32 v6, v6, v4
	v_mov_b32_e32 v5, s9
	v_add3_u32 v3, v4, v3, v6
	ds_write_b32 v5, v3
	v_mov_b32_e32 v4, v118
	v_readlane_b32 s9, v254, 60
	s_nop 0
	v_add_u32_e32 v4, 0x13f, v4
	v_mul_hi_i32 v6, v4, s8
	v_lshrrev_b32_e32 v7, 31, v6
	v_ashrrev_i32_e32 v6, 7, v6
	v_add_u32_e32 v6, v6, v7
	v_mul_lo_u32 v6, v6, s2
	v_sub_u32_e32 v6, v6, v4
	v_mov_b32_e32 v5, s9
	v_add3_u32 v3, v4, v3, v6
	ds_write_b32 v5, v3
	v_mov_b32_e32 v4, v119
	v_readlane_b32 s9, v254, 61
	s_nop 0
	v_add_u32_e32 v4, 0x13f, v4
	v_mul_hi_i32 v6, v4, s8
	v_lshrrev_b32_e32 v7, 31, v6
	v_ashrrev_i32_e32 v6, 7, v6
	v_add_u32_e32 v6, v6, v7
	v_mul_lo_u32 v6, v6, s2
	v_sub_u32_e32 v6, v6, v4
	v_mov_b32_e32 v5, s9
	v_add3_u32 v3, v4, v3, v6
	ds_write_b32 v5, v3
	v_mov_b32_e32 v4, v120
	v_readlane_b32 s9, v254, 62
	s_nop 0
	v_add_u32_e32 v4, 0x13f, v4
	v_mul_hi_i32 v6, v4, s8
	v_lshrrev_b32_e32 v7, 31, v6
	v_ashrrev_i32_e32 v6, 7, v6
	v_add_u32_e32 v6, v6, v7
	v_mul_lo_u32 v6, v6, s2
	v_sub_u32_e32 v6, v6, v4
	v_mov_b32_e32 v5, s9
	v_add3_u32 v3, v4, v3, v6
	ds_write_b32 v5, v3
	v_mov_b32_e32 v4, v121
	v_readlane_b32 s9, v254, 63
	s_nop 0
	v_add_u32_e32 v4, 0x13f, v4
	v_mul_hi_i32 v6, v4, s8
	v_lshrrev_b32_e32 v7, 31, v6
	v_ashrrev_i32_e32 v6, 7, v6
	v_add_u32_e32 v6, v6, v7
	v_mul_lo_u32 v6, v6, s2
	v_sub_u32_e32 v6, v6, v4
	v_mov_b32_e32 v5, s9
	v_add3_u32 v3, v4, v3, v6
	ds_write_b32 v5, v3
	v_mov_b32_e32 v4, v122
	v_readlane_b32 s9, v255, 0
	s_nop 0
	v_add_u32_e32 v4, 0x13f, v4
	v_mul_hi_i32 v6, v4, s8
	v_lshrrev_b32_e32 v7, 31, v6
	v_ashrrev_i32_e32 v6, 7, v6
	v_add_u32_e32 v6, v6, v7
	v_mul_lo_u32 v6, v6, s2
	v_sub_u32_e32 v6, v6, v4
	v_mov_b32_e32 v5, s9
	v_add3_u32 v3, v4, v3, v6
	ds_write_b32 v5, v3
	v_mov_b32_e32 v4, v123
	v_readlane_b32 s9, v255, 1
	s_nop 0
	v_add_u32_e32 v4, 0x13f, v4
	v_mul_hi_i32 v6, v4, s8
	v_lshrrev_b32_e32 v7, 31, v6
	v_ashrrev_i32_e32 v6, 7, v6
	v_add_u32_e32 v6, v6, v7
	v_mul_lo_u32 v6, v6, s2
	v_sub_u32_e32 v6, v6, v4
	v_mov_b32_e32 v5, s9
	v_add3_u32 v3, v4, v3, v6
	ds_write_b32 v5, v3
	v_mov_b32_e32 v4, v124
	v_readlane_b32 s9, v255, 2
	s_nop 0
	v_add_u32_e32 v4, 0x13f, v4
	v_mul_hi_i32 v6, v4, s8
	v_lshrrev_b32_e32 v7, 31, v6
	v_ashrrev_i32_e32 v6, 7, v6
	v_add_u32_e32 v6, v6, v7
	v_mul_lo_u32 v6, v6, s2
	v_sub_u32_e32 v6, v6, v4
	v_mov_b32_e32 v5, s9
	v_add3_u32 v3, v4, v3, v6
	ds_write_b32 v5, v3
	v_mov_b32_e32 v4, v125
	v_readlane_b32 s9, v255, 3
	s_nop 0
	v_add_u32_e32 v4, 0x13f, v4
	v_mul_hi_i32 v6, v4, s8
	v_lshrrev_b32_e32 v7, 31, v6
	v_ashrrev_i32_e32 v6, 7, v6
	v_add_u32_e32 v6, v6, v7
	v_mul_lo_u32 v6, v6, s2
	v_sub_u32_e32 v6, v6, v4
	v_mov_b32_e32 v5, s9
	v_add3_u32 v3, v4, v3, v6
	ds_write_b32 v5, v3
	v_mov_b32_e32 v4, v126
	v_readlane_b32 s9, v255, 4
	s_nop 0
	v_add_u32_e32 v4, 0x13f, v4
	v_mul_hi_i32 v6, v4, s8
	v_lshrrev_b32_e32 v7, 31, v6
	v_ashrrev_i32_e32 v6, 7, v6
	v_add_u32_e32 v6, v6, v7
	v_mul_lo_u32 v6, v6, s2
	v_sub_u32_e32 v6, v6, v4
	v_mov_b32_e32 v5, s9
	v_add3_u32 v3, v4, v3, v6
	ds_write_b32 v5, v3
	v_mov_b32_e32 v4, v127
	v_readlane_b32 s9, v255, 5
	s_nop 0
	v_add_u32_e32 v4, 0x13f, v4
	v_mul_hi_i32 v6, v4, s8
	v_lshrrev_b32_e32 v7, 31, v6
	v_ashrrev_i32_e32 v6, 7, v6
	v_add_u32_e32 v6, v6, v7
	v_mul_lo_u32 v6, v6, s2
	v_sub_u32_e32 v6, v6, v4
	v_mov_b32_e32 v5, s9
	v_add3_u32 v3, v4, v3, v6
	ds_write_b32 v5, v3
	v_mov_b32_e32 v4, v128
	v_readlane_b32 s9, v255, 6
	s_nop 0
	v_add_u32_e32 v4, 0x13f, v4
	v_mul_hi_i32 v6, v4, s8
	v_lshrrev_b32_e32 v7, 31, v6
	v_ashrrev_i32_e32 v6, 7, v6
	v_add_u32_e32 v6, v6, v7
	v_mul_lo_u32 v6, v6, s2
	v_sub_u32_e32 v6, v6, v4
	v_mov_b32_e32 v5, s9
	v_add3_u32 v3, v4, v3, v6
	ds_write_b32 v5, v3
	v_mov_b32_e32 v4, v129
	v_readlane_b32 s9, v255, 7
	s_nop 0
	v_add_u32_e32 v4, 0x13f, v4
	v_mul_hi_i32 v6, v4, s8
	v_lshrrev_b32_e32 v7, 31, v6
	v_ashrrev_i32_e32 v6, 7, v6
	v_add_u32_e32 v6, v6, v7
	v_mul_lo_u32 v6, v6, s2
	v_sub_u32_e32 v6, v6, v4
	v_mov_b32_e32 v5, s9
	v_add3_u32 v3, v4, v3, v6
	ds_write_b32 v5, v3
	v_mov_b32_e32 v4, v130
	v_readlane_b32 s9, v255, 8
	s_nop 0
	v_add_u32_e32 v4, 0x13f, v4
	v_mul_hi_i32 v6, v4, s8
	v_lshrrev_b32_e32 v7, 31, v6
	v_ashrrev_i32_e32 v6, 7, v6
	v_add_u32_e32 v6, v6, v7
	v_mul_lo_u32 v6, v6, s2
	v_sub_u32_e32 v6, v6, v4
	v_mov_b32_e32 v5, s9
	v_add3_u32 v3, v4, v3, v6
	ds_write_b32 v5, v3
	v_mov_b32_e32 v0, v131
	s_nop 0
	v_add_u32_e32 v0, 0x13f, v0
	v_mul_hi_i32 v1, v0, s8
	v_lshrrev_b32_e32 v4, 31, v1
	v_ashrrev_i32_e32 v1, 7, v1
	v_add_u32_e32 v1, v1, v4
	v_mul_lo_u32 v1, v1, s2
	v_sub_u32_e32 v1, v1, v0
	v_readlane_b32 s2, v254, 2
	v_add3_u32 v0, v0, v3, v1
	s_nop 0
	v_mov_b32_e32 v1, s2
	ds_write_b32 v1, v0

.LBB0_1051:
	s_ashr_i32 s2, s16, 31
	s_lshr_b32 s2, s2, 25
	s_add_i32 s2, s16, s2
	s_ashr_i32 s12, s2, 7
	s_and_b32 s2, s2, 0xffffff80
	s_sub_i32 s2, s16, s2
	s_lshl_b32 s12, s12, 3
	s_and_b32 s13, s2, 7
	s_or_b32 s20, s12, s13
	v_cmp_ge_i32_e32 vcc, s20, v158
	s_cbranch_vccnz .LBB0_1050
	s_lshl_b32 s12, s20, 2
	s_add_i32 s12, s12, 0
	s_add_i32 s12, s12, 0x20b40
	v_mov_b32_e32 v0, s12
	v_mov_b32_e32 v2, v145
	s_mulk_i32 s20, 0x140
	ds_read_b32 v0, v0
	s_mov_b64 s[12:13], s[0:1]
	s_mov_b64 s[22:23], 0
	s_mov_b64 s[24:25], s[4:5]
	v_add3_u32 v144, s20, v159, v2
	s_mul_i32 s14, s2, 5
	v_lshlrev_b64 v[4:5], 10, v[144:145]
	s_lshl_b32 s2, s2, 4
	v_lshl_add_u64 v[4:5], s[12:13], 0, v[4:5]
	v_mov_b32_e32 v101, v145
	s_and_b32 s12, s2, 0xffffff80
	s_and_b32 s2, s14, 7
	v_lshl_add_u64 v[108:109], v[4:5], 0, v[100:101]
	s_lshl_b32 s36, s2, 7
	v_lshl_add_u64 v[16:17], v[108:109], 0, s[36:37]
	s_waitcnt lgkmcnt(0)
	v_ashrrev_i32_e32 v1, 31, v0
	v_add_co_u32_e32 v4, vcc, s70, v16
	v_lshlrev_b64 v[0:1], 22, v[0:1]
	s_ashr_i32 s13, s12, 31
	v_addc_co_u32_e32 v5, vcc, 0, v17, vcc
	v_lshl_add_u64 v[0:1], s[24:25], 0, v[0:1]
	s_lshl_b64 s[22:23], s[12:13], 2
	v_add_co_u32_e32 v8, vcc, s83, v16
	v_lshl_add_u64 v[0:1], v[0:1], 0, s[22:23]
	v_mov_b32_e32 v103, v145
	v_addc_co_u32_e32 v9, vcc, 0, v17, vcc
	v_lshl_add_u64 v[0:1], v[0:1], 0, v[102:103]
	v_ashrrev_i32_e32 v3, 31, v2
	v_add_co_u32_e32 v12, vcc, s3, v16
	v_lshl_add_u64 v[0:1], v[2:3], 2, v[0:1]
	s_nop 0
	v_addc_co_u32_e32 v13, vcc, 0, v17, vcc
	v_lshl_add_u64 v[110:111], v[0:1], 0, s[10:11]
	v_add_u32_e32 v200, s20, v160
	v_mov_b32_e32 v201, v145
	v_lshl_add_u64 v[202:203], v[200:201], 2, s[8:9]
	global_load_dword v190, v[202:203], off
	global_load_dword v192, v[202:203], off offset:64
	global_load_dword v194, v[202:203], off offset:128
	global_load_dword v196, v[202:203], off offset:192
	global_load_dword v198, v[202:203], off offset:256
	global_load_dwordx4 v[0:3], v[16:17], off
	s_nop 0
	global_load_dwordx4 v[4:7], v[4:5], off
	v_add_co_u32_e32 v16, vcc, s53, v16
	s_lshl_b32 s36, s2, 19
	s_nop 0
	v_addc_co_u32_e32 v17, vcc, 0, v17, vcc
	global_load_dwordx4 v[8:11], v[8:9], off
	s_nop 0
	global_load_dwordx4 v[12:15], v[12:13], off
	global_load_dwordx4 v[16:19], v[16:17], off
	v_lshl_add_u64 v[32:33], v[110:111], 0, s[36:37]
	v_add_co_u32_e32 v34, vcc, 0x2000, v32
	s_nop 1
	v_addc_co_u32_e32 v35, vcc, 0, v33, vcc
	v_add_co_u32_e32 v28, vcc, 0x4000, v32
	s_nop 1
	v_addc_co_u32_e32 v29, vcc, 0, v33, vcc
	v_add_co_u32_e32 v30, vcc, 0x6000, v32
	s_nop 1
	v_addc_co_u32_e32 v31, vcc, 0, v33, vcc
	global_load_dwordx4 v[20:23], v[32:33], off
	global_load_dwordx4 v[24:27], v[34:35], off
	global_load_dwordx4 v[32:35], v[30:31], off
	global_load_dwordx4 v[28:31], v[28:29], off
	s_nop 0
	s_add_i32 s2, s14, 1
	s_nop 0
	s_nop 0
	s_nop 0
	s_nop 0
	s_and_b32 s2, s2, 7
	s_nop 0
	s_lshl_b32 s36, s2, 19
	s_nop 0
	s_nop 0
	s_nop 0
	s_nop 0
	s_nop 0
	v_lshl_add_u64 v[124:125], v[110:111], 0, s[36:37]
	v_add_co_u32_e32 v126, vcc, 0x2000, v124
	s_nop 1
	v_addc_co_u32_e32 v127, vcc, 0, v125, vcc
	v_add_co_u32_e32 v120, vcc, 0x4000, v124
	s_nop 1
	v_addc_co_u32_e32 v121, vcc, 0, v125, vcc
	v_add_co_u32_e32 v122, vcc, 0x6000, v124
	s_nop 1
	v_addc_co_u32_e32 v123, vcc, 0, v125, vcc
	global_load_dwordx4 v[112:115], v[124:125], off
	global_load_dwordx4 v[116:119], v[126:127], off
	global_load_dwordx4 v[124:127], v[122:123], off
	global_load_dwordx4 v[120:123], v[120:121], off
	v_add_u32_e32 v101, s66, v164
	s_nop 0
	s_lshl_b32 s36, s2, 7
	s_nop 0
	v_add_u32_e32 v103, s66, v163
	s_nop 0
	v_mov_b32_e32 v64, 0
	s_nop 0
	s_mov_b32 s15, -2
	s_nop 0
	v_mov_b32_e32 v65, v64
	s_nop 0
	v_mov_b32_e32 v66, v64
	s_nop 0
	s_waitcnt vmcnt(0)
	ds_write_b128 v165, v[0:3]
	ds_write_b128 v165, v[4:7] offset:8192
	ds_write_b128 v165, v[8:11] offset:16384
	ds_write_b128 v165, v[12:15] offset:24576
	ds_write_b128 v165, v[16:19] offset:32768
	v_mov_b32_e32 v67, v64
	v_mov_b32_e32 v68, v64
	v_mov_b32_e32 v69, v64
	v_mov_b32_e32 v70, v64
	v_mov_b32_e32 v71, v64
	v_mov_b32_e32 v72, v64
	v_mov_b32_e32 v73, v64
	v_mov_b32_e32 v74, v64
	v_mov_b32_e32 v75, v64
	v_mov_b32_e32 v76, v64
	v_mov_b32_e32 v77, v64
	v_permlane32_swap_b32_e32 v20, v22
	v_permlane32_swap_b32_e32 v21, v23
	v_permlane32_swap_b32_e32 v24, v26
	v_permlane32_swap_b32_e32 v25, v27
	v_permlane32_swap_b32_e32 v28, v30
	v_permlane32_swap_b32_e32 v29, v31
	v_permlane32_swap_b32_e32 v32, v34
	v_permlane32_swap_b32_e32 v33, v35
	v_cvt_pk_bf16_f32 v0, v20, v24
	v_cvt_pk_bf16_f32 v1, v28, v32
	v_cvt_pk_bf16_f32 v2, v22, v26
	v_cvt_pk_bf16_f32 v3, v30, v34
	v_cvt_pk_bf16_f32 v4, v21, v25
	v_cvt_pk_bf16_f32 v5, v29, v33
	v_cvt_pk_bf16_f32 v6, v23, v27
	v_cvt_pk_bf16_f32 v7, v31, v35
	v_mov_b32_e32 v78, v64
	v_mov_b32_e32 v79, v64
	v_mov_b32_e32 v48, v64
	v_mov_b32_e32 v49, v64
	v_mov_b32_e32 v50, v64
	v_mov_b32_e32 v51, v64
	v_mov_b32_e32 v52, v64
	v_mov_b32_e32 v53, v64
	v_mov_b32_e32 v54, v64
	v_mov_b32_e32 v55, v64
	v_mov_b32_e32 v56, v64
	v_mov_b32_e32 v57, v64
	v_mov_b32_e32 v58, v64
	v_mov_b32_e32 v59, v64
	ds_write_b128 v101, v[0:3]
	v_lshl_add_u64 v[0:1], v[108:109], 0, s[36:37]
	v_add_co_u32_e32 v2, vcc, s70, v0
	ds_write_b128 v103, v[4:7]
	s_nop 0
	v_addc_co_u32_e32 v3, vcc, 0, v1, vcc
	global_load_dwordx4 v[80:83], v[0:1], off
	global_load_dwordx4 v[84:87], v[2:3], off
	v_add_co_u32_e32 v2, vcc, s83, v0
	v_mov_b32_e32 v60, v64
	s_nop 0
	v_addc_co_u32_e32 v3, vcc, 0, v1, vcc
	v_add_co_u32_e32 v4, vcc, 0x30000, v0
	v_mov_b32_e32 v61, v64
	s_nop 0
	v_addc_co_u32_e32 v5, vcc, 0, v1, vcc
	v_add_co_u32_e32 v0, vcc, 0x40000, v0
	global_load_dwordx4 v[88:91], v[2:3], off
	global_load_dwordx4 v[92:95], v[4:5], off
	v_addc_co_u32_e32 v1, vcc, 0, v1, vcc
	global_load_dwordx4 v[96:99], v[0:1], off
	v_mov_b32_e32 v62, v64
	v_mov_b32_e32 v63, v64
	v_mov_b32_e32 v32, v64
	v_mov_b32_e32 v33, v64
	v_mov_b32_e32 v34, v64
	v_mov_b32_e32 v35, v64
	v_mov_b32_e32 v36, v64
	v_mov_b32_e32 v37, v64
	v_mov_b32_e32 v38, v64
	v_mov_b32_e32 v39, v64
	v_mov_b32_e32 v40, v64
	v_mov_b32_e32 v41, v64
	v_mov_b32_e32 v42, v64
	v_mov_b32_e32 v43, v64
	v_mov_b32_e32 v44, v64
	v_mov_b32_e32 v45, v64
	v_mov_b32_e32 v46, v64
	v_mov_b32_e32 v47, v64
	v_mov_b32_e32 v16, v64
	v_mov_b32_e32 v17, v64
	v_mov_b32_e32 v18, v64
	v_mov_b32_e32 v19, v64
	v_mov_b32_e32 v20, v64
	v_mov_b32_e32 v21, v64
	v_mov_b32_e32 v22, v64
	v_mov_b32_e32 v23, v64
	v_mov_b32_e32 v24, v64
	v_mov_b32_e32 v25, v64
	v_mov_b32_e32 v26, v64
	v_mov_b32_e32 v27, v64
	v_mov_b32_e32 v28, v64
	v_mov_b32_e32 v29, v64
	v_mov_b32_e32 v30, v64
	v_mov_b32_e32 v31, v64
	v_mov_b32_e32 v0, v64
	v_mov_b32_e32 v1, v64
	v_mov_b32_e32 v2, v64
	v_mov_b32_e32 v3, v64
	v_mov_b32_e32 v4, v64
	v_mov_b32_e32 v5, v64
	v_mov_b32_e32 v6, v64
	v_mov_b32_e32 v7, v64
	v_mov_b32_e32 v8, v64
	v_mov_b32_e32 v9, v64
	v_mov_b32_e32 v10, v64
	v_mov_b32_e32 v11, v64
	v_mov_b32_e32 v12, v64
	v_mov_b32_e32 v13, v64
	v_mov_b32_e32 v14, v64
	v_mov_b32_e32 v15, v64
	s_waitcnt lgkmcnt(0)
	s_barrier
.LBB0_1053:
	s_add_i32 s2, s14, s15
	s_add_i32 s21, s2, 4
	s_and_b32 s21, s21, 7
	s_lshl_b32 s36, s21, 19
	v_add_u32_e32 v105, v166, v162
	s_nop 0
	s_nop 1
	s_nop 1
	s_nop 1
	s_nop 1
	s_nop 1
	v_lshl_add_u64 v[140:141], v[110:111], 0, s[36:37]
	v_add_co_u32_e32 v142, vcc, 0x2000, v140
	s_nop 1
	v_addc_co_u32_e32 v143, vcc, 0, v141, vcc
	v_add_co_u32_e32 v136, vcc, 0x4000, v140
	s_nop 1
	v_addc_co_u32_e32 v137, vcc, 0, v141, vcc
	v_add_co_u32_e32 v138, vcc, 0x6000, v140
	s_nop 1
	v_addc_co_u32_e32 v139, vcc, 0, v141, vcc
	global_load_dwordx4 v[128:131], v[140:141], off
	global_load_dwordx4 v[132:135], v[142:143], off
	global_load_dwordx4 v[140:143], v[138:139], off
	global_load_dwordx4 v[136:139], v[136:137], off
	ds_read_b128 v[146:149], v105
	ds_read_b128 v[150:153], v105 offset:2048
	ds_read_b128 v[154:157], v105 offset:4096
	ds_read_b128 v[170:173], v105 offset:6144
	v_add_u32_e32 v105, v167, v162
	ds_read_b128 v[174:177], v105
	ds_read_b128 v[178:181], v105 offset:2048
	s_setprio 1
	s_waitcnt lgkmcnt(1)
	v_mfma_f32_16x16x32_bf16 v[76:79], v[146:149], v[174:177], v[76:79]
	v_mfma_f32_16x16x32_bf16 v[72:75], v[150:153], v[174:177], v[72:75]
	v_mfma_f32_16x16x32_bf16 v[68:71], v[154:157], v[174:177], v[68:71]
	v_mfma_f32_16x16x32_bf16 v[64:67], v[170:173], v[174:177], v[64:67]
	s_setprio 0
	ds_read_b128 v[174:177], v105 offset:4096
	s_setprio 1
	s_waitcnt lgkmcnt(1)
	v_mfma_f32_16x16x32_bf16 v[48:51], v[146:149], v[178:181], v[48:51]
	v_mfma_f32_16x16x32_bf16 v[52:55], v[150:153], v[178:181], v[52:55]
	v_mfma_f32_16x16x32_bf16 v[56:59], v[154:157], v[178:181], v[56:59]
	v_mfma_f32_16x16x32_bf16 v[60:63], v[170:173], v[178:181], v[60:63]
	s_setprio 0
	ds_read_b128 v[178:181], v105 offset:6144
	s_setprio 1
	s_waitcnt lgkmcnt(1)
	v_mfma_f32_16x16x32_bf16 v[32:35], v[146:149], v[174:177], v[32:35]
	v_mfma_f32_16x16x32_bf16 v[36:39], v[150:153], v[174:177], v[36:39]
	v_mfma_f32_16x16x32_bf16 v[40:43], v[154:157], v[174:177], v[40:43]
	v_mfma_f32_16x16x32_bf16 v[44:47], v[170:173], v[174:177], v[44:47]
	s_setprio 0
	ds_read_b128 v[174:177], v105 offset:8192
	s_setprio 1
	s_waitcnt lgkmcnt(1)
	v_mfma_f32_16x16x32_bf16 v[16:19], v[146:149], v[178:181], v[16:19]
	v_mfma_f32_16x16x32_bf16 v[20:23], v[150:153], v[178:181], v[20:23]
	v_mfma_f32_16x16x32_bf16 v[24:27], v[154:157], v[178:181], v[24:27]
	v_mfma_f32_16x16x32_bf16 v[28:31], v[170:173], v[178:181], v[28:31]
	s_setprio 0
	s_setprio 1
	s_waitcnt lgkmcnt(0)
	v_mfma_f32_16x16x32_bf16 v[0:3], v[146:149], v[174:177], v[0:3]
	v_mfma_f32_16x16x32_bf16 v[4:7], v[150:153], v[174:177], v[4:7]
	v_mfma_f32_16x16x32_bf16 v[8:11], v[154:157], v[174:177], v[8:11]
	v_mfma_f32_16x16x32_bf16 v[12:15], v[170:173], v[174:177], v[12:15]
	s_setprio 0
	v_add_u32_e32 v107, v166, v161
	ds_read_b128 v[146:149], v107
	ds_read_b128 v[150:153], v107 offset:2048
	ds_read_b128 v[154:157], v107 offset:4096
	ds_read_b128 v[170:173], v107 offset:6144
	v_add_u32_e32 v107, v167, v161
	ds_read_b128 v[174:177], v107
	ds_read_b128 v[178:181], v107 offset:2048
	s_setprio 1
	s_waitcnt lgkmcnt(1)
	v_mfma_f32_16x16x32_bf16 v[76:79], v[146:149], v[174:177], v[76:79]
	v_mfma_f32_16x16x32_bf16 v[72:75], v[150:153], v[174:177], v[72:75]
	v_mfma_f32_16x16x32_bf16 v[68:71], v[154:157], v[174:177], v[68:71]
	v_mfma_f32_16x16x32_bf16 v[64:67], v[170:173], v[174:177], v[64:67]
	s_setprio 0
	ds_read_b128 v[174:177], v107 offset:4096
	s_setprio 1
	s_waitcnt lgkmcnt(1)
	v_mfma_f32_16x16x32_bf16 v[48:51], v[146:149], v[178:181], v[48:51]
	v_mfma_f32_16x16x32_bf16 v[52:55], v[150:153], v[178:181], v[52:55]
	v_mfma_f32_16x16x32_bf16 v[56:59], v[154:157], v[178:181], v[56:59]
	v_mfma_f32_16x16x32_bf16 v[60:63], v[170:173], v[178:181], v[60:63]
	s_setprio 0
	ds_read_b128 v[178:181], v107 offset:6144
	s_setprio 1
	s_waitcnt lgkmcnt(1)
	v_mfma_f32_16x16x32_bf16 v[32:35], v[146:149], v[174:177], v[32:35]
	v_mfma_f32_16x16x32_bf16 v[36:39], v[150:153], v[174:177], v[36:39]
	v_mfma_f32_16x16x32_bf16 v[40:43], v[154:157], v[174:177], v[40:43]
	v_mfma_f32_16x16x32_bf16 v[44:47], v[170:173], v[174:177], v[44:47]
	s_setprio 0
	ds_read_b128 v[174:177], v107 offset:8192
	s_setprio 1
	s_waitcnt lgkmcnt(1)
	v_mfma_f32_16x16x32_bf16 v[16:19], v[146:149], v[178:181], v[16:19]
	v_mfma_f32_16x16x32_bf16 v[20:23], v[150:153], v[178:181], v[20:23]
	v_mfma_f32_16x16x32_bf16 v[24:27], v[154:157], v[178:181], v[24:27]
	v_mfma_f32_16x16x32_bf16 v[28:31], v[170:173], v[178:181], v[28:31]
	s_setprio 0
	s_setprio 1
	s_waitcnt lgkmcnt(0)
	v_mfma_f32_16x16x32_bf16 v[0:3], v[146:149], v[174:177], v[0:3]
	v_mfma_f32_16x16x32_bf16 v[4:7], v[150:153], v[174:177], v[4:7]
	v_mfma_f32_16x16x32_bf16 v[8:11], v[154:157], v[174:177], v[8:11]
	v_mfma_f32_16x16x32_bf16 v[12:15], v[170:173], v[174:177], v[12:15]
	s_setprio 0
	s_waitcnt vmcnt(8)
	ds_write_b128 v165, v[80:83] offset:40960
	s_waitcnt vmcnt(7)
	ds_write_b128 v165, v[84:87] offset:49152
	s_waitcnt vmcnt(6)
	ds_write_b128 v165, v[88:91] offset:57344
	s_waitcnt vmcnt(5)
	ds_write_b128 v168, v[92:95] offset:24576
	s_waitcnt vmcnt(4)
	ds_write_b128 v168, v[96:99] offset:32768
	v_permlane32_swap_b32_e32 v112, v114
	v_permlane32_swap_b32_e32 v113, v115
	v_permlane32_swap_b32_e32 v116, v118
	v_permlane32_swap_b32_e32 v117, v119
	v_permlane32_swap_b32_e32 v120, v122
	v_permlane32_swap_b32_e32 v121, v123
	v_permlane32_swap_b32_e32 v124, v126
	v_permlane32_swap_b32_e32 v125, v127
	v_cvt_pk_bf16_f32 v80, v112, v116
	v_cvt_pk_bf16_f32 v81, v120, v124
	v_cvt_pk_bf16_f32 v82, v114, v118
	v_cvt_pk_bf16_f32 v83, v122, v126
	v_cvt_pk_bf16_f32 v84, v113, v117
	v_cvt_pk_bf16_f32 v85, v121, v125
	v_cvt_pk_bf16_f32 v86, v115, v119
	v_cvt_pk_bf16_f32 v87, v123, v127
	v_add_u32_e32 v88, s18, v164
	s_lshl_b32 s36, s21, 7
	v_add_u32_e32 v89, s18, v163
	ds_write_b128 v88, v[80:83]
	ds_write_b128 v89, v[84:87]
	v_lshl_add_u64 v[80:81], v[108:109], 0, s[36:37]
	v_add_co_u32_e32 v84, vcc, s70, v80
	s_add_i32 s2, s2, 5
	s_nop 0
	v_addc_co_u32_e32 v85, vcc, 0, v81, vcc
	v_add_co_u32_e32 v88, vcc, s83, v80
	s_and_b32 s21, s2, 7
	s_nop 0
	v_addc_co_u32_e32 v89, vcc, 0, v81, vcc
	v_add_co_u32_e32 v92, vcc, s3, v80
	s_lshl_b32 s36, s21, 19
	s_nop 0
	v_addc_co_u32_e32 v93, vcc, 0, v81, vcc
	v_add_co_u32_e32 v96, vcc, s53, v80
	s_nop 0
	v_addc_co_u32_e32 v97, vcc, 0, v81, vcc
	global_load_dwordx4 v[80:83], v[80:81], off
	s_nop 0
	global_load_dwordx4 v[84:87], v[84:85], off
	s_nop 0
	global_load_dwordx4 v[88:91], v[88:89], off
	s_nop 0
	global_load_dwordx4 v[92:95], v[92:93], off
	s_nop 0
	global_load_dwordx4 v[96:99], v[96:97], off
	v_lshl_add_u64 v[124:125], v[110:111], 0, s[36:37]
	v_add_co_u32_e32 v126, vcc, 0x2000, v124
	s_nop 1
	v_addc_co_u32_e32 v127, vcc, 0, v125, vcc
	v_add_co_u32_e32 v120, vcc, 0x4000, v124
	s_nop 1
	v_addc_co_u32_e32 v121, vcc, 0, v125, vcc
	v_add_co_u32_e32 v122, vcc, 0x6000, v124
	s_nop 1
	v_addc_co_u32_e32 v123, vcc, 0, v125, vcc
	s_waitcnt lgkmcnt(0)
	s_nop 0
	s_barrier
	s_nop 1
	v_add_u32_e32 v144, v169, v162
	s_nop 1
	s_nop 1
	global_load_dwordx4 v[112:115], v[124:125], off
	global_load_dwordx4 v[116:119], v[126:127], off
	global_load_dwordx4 v[124:127], v[122:123], off
	global_load_dwordx4 v[120:123], v[120:121], off
	ds_read_b128 v[146:149], v144
	ds_read_b128 v[150:153], v144 offset:2048
	ds_read_b128 v[154:157], v144 offset:4096
	ds_read_b128 v[170:173], v144 offset:6144
	ds_read_b128 v[174:177], v105 offset:40960
	ds_read_b128 v[178:181], v105 offset:43008
	s_setprio 1
	s_waitcnt lgkmcnt(1)
	v_mfma_f32_16x16x32_bf16 v[76:79], v[146:149], v[174:177], v[76:79]
	v_mfma_f32_16x16x32_bf16 v[72:75], v[150:153], v[174:177], v[72:75]
	v_mfma_f32_16x16x32_bf16 v[68:71], v[154:157], v[174:177], v[68:71]
	v_mfma_f32_16x16x32_bf16 v[64:67], v[170:173], v[174:177], v[64:67]
	s_setprio 0
	ds_read_b128 v[174:177], v105 offset:45056
	s_setprio 1
	s_waitcnt lgkmcnt(1)
	v_mfma_f32_16x16x32_bf16 v[48:51], v[146:149], v[178:181], v[48:51]
	v_mfma_f32_16x16x32_bf16 v[52:55], v[150:153], v[178:181], v[52:55]
	v_mfma_f32_16x16x32_bf16 v[56:59], v[154:157], v[178:181], v[56:59]
	v_mfma_f32_16x16x32_bf16 v[60:63], v[170:173], v[178:181], v[60:63]
	s_setprio 0
	ds_read_b128 v[178:181], v105 offset:47104
	s_setprio 1
	s_waitcnt lgkmcnt(1)
	v_mfma_f32_16x16x32_bf16 v[32:35], v[146:149], v[174:177], v[32:35]
	v_mfma_f32_16x16x32_bf16 v[36:39], v[150:153], v[174:177], v[36:39]
	v_mfma_f32_16x16x32_bf16 v[40:43], v[154:157], v[174:177], v[40:43]
	v_mfma_f32_16x16x32_bf16 v[44:47], v[170:173], v[174:177], v[44:47]
	s_setprio 0
	ds_read_b128 v[174:177], v105 offset:49152
	s_setprio 1
	s_waitcnt lgkmcnt(1)
	v_mfma_f32_16x16x32_bf16 v[16:19], v[146:149], v[178:181], v[16:19]
	v_mfma_f32_16x16x32_bf16 v[20:23], v[150:153], v[178:181], v[20:23]
	v_mfma_f32_16x16x32_bf16 v[24:27], v[154:157], v[178:181], v[24:27]
	v_mfma_f32_16x16x32_bf16 v[28:31], v[170:173], v[178:181], v[28:31]
	s_setprio 0
	s_setprio 1
	s_waitcnt lgkmcnt(0)
	v_mfma_f32_16x16x32_bf16 v[0:3], v[146:149], v[174:177], v[0:3]
	v_mfma_f32_16x16x32_bf16 v[4:7], v[150:153], v[174:177], v[4:7]
	v_mfma_f32_16x16x32_bf16 v[8:11], v[154:157], v[174:177], v[8:11]
	v_mfma_f32_16x16x32_bf16 v[12:15], v[170:173], v[174:177], v[12:15]
	s_setprio 0
	v_add_u32_e32 v105, v169, v161
	ds_read_b128 v[146:149], v105
	ds_read_b128 v[150:153], v105 offset:2048
	ds_read_b128 v[154:157], v105 offset:4096
	ds_read_b128 v[170:173], v105 offset:6144
	ds_read_b128 v[174:177], v107 offset:40960
	ds_read_b128 v[178:181], v107 offset:43008
	s_setprio 1
	s_waitcnt lgkmcnt(1)
	v_mfma_f32_16x16x32_bf16 v[76:79], v[146:149], v[174:177], v[76:79]
	v_mfma_f32_16x16x32_bf16 v[72:75], v[150:153], v[174:177], v[72:75]
	v_mfma_f32_16x16x32_bf16 v[68:71], v[154:157], v[174:177], v[68:71]
	v_mfma_f32_16x16x32_bf16 v[64:67], v[170:173], v[174:177], v[64:67]
	s_setprio 0
	ds_read_b128 v[174:177], v107 offset:45056
	s_setprio 1
	s_waitcnt lgkmcnt(1)
	v_mfma_f32_16x16x32_bf16 v[48:51], v[146:149], v[178:181], v[48:51]
	v_mfma_f32_16x16x32_bf16 v[52:55], v[150:153], v[178:181], v[52:55]
	v_mfma_f32_16x16x32_bf16 v[56:59], v[154:157], v[178:181], v[56:59]
	v_mfma_f32_16x16x32_bf16 v[60:63], v[170:173], v[178:181], v[60:63]
	s_setprio 0
	ds_read_b128 v[178:181], v107 offset:47104
	s_setprio 1
	s_waitcnt lgkmcnt(1)
	v_mfma_f32_16x16x32_bf16 v[32:35], v[146:149], v[174:177], v[32:35]
	v_mfma_f32_16x16x32_bf16 v[36:39], v[150:153], v[174:177], v[36:39]
	v_mfma_f32_16x16x32_bf16 v[40:43], v[154:157], v[174:177], v[40:43]
	v_mfma_f32_16x16x32_bf16 v[44:47], v[170:173], v[174:177], v[44:47]
	s_setprio 0
	ds_read_b128 v[174:177], v107 offset:49152
	s_setprio 1
	s_waitcnt lgkmcnt(1)
	v_mfma_f32_16x16x32_bf16 v[16:19], v[146:149], v[178:181], v[16:19]
	v_mfma_f32_16x16x32_bf16 v[20:23], v[150:153], v[178:181], v[20:23]
	v_mfma_f32_16x16x32_bf16 v[24:27], v[154:157], v[178:181], v[24:27]
	v_mfma_f32_16x16x32_bf16 v[28:31], v[170:173], v[178:181], v[28:31]
	s_setprio 0
	s_setprio 1
	s_waitcnt lgkmcnt(0)
	v_mfma_f32_16x16x32_bf16 v[0:3], v[146:149], v[174:177], v[0:3]
	v_mfma_f32_16x16x32_bf16 v[4:7], v[150:153], v[174:177], v[4:7]
	v_mfma_f32_16x16x32_bf16 v[8:11], v[154:157], v[174:177], v[8:11]
	v_mfma_f32_16x16x32_bf16 v[12:15], v[170:173], v[174:177], v[12:15]
	s_setprio 0
	s_lshl_b32 s36, s21, 7
	s_waitcnt vmcnt(8)
	ds_write_b128 v165, v[80:83]
	s_waitcnt vmcnt(7)
	ds_write_b128 v165, v[84:87] offset:8192
	s_waitcnt vmcnt(6)
	ds_write_b128 v165, v[88:91] offset:16384
	s_waitcnt vmcnt(5)
	ds_write_b128 v165, v[92:95] offset:24576
	s_waitcnt vmcnt(4)
	ds_write_b128 v165, v[96:99] offset:32768
	v_permlane32_swap_b32_e32 v128, v130
	v_permlane32_swap_b32_e32 v129, v131
	v_permlane32_swap_b32_e32 v132, v134
	v_permlane32_swap_b32_e32 v133, v135
	v_permlane32_swap_b32_e32 v136, v138
	v_permlane32_swap_b32_e32 v137, v139
	v_permlane32_swap_b32_e32 v140, v142
	v_permlane32_swap_b32_e32 v141, v143
	v_cvt_pk_bf16_f32 v80, v128, v132
	v_cvt_pk_bf16_f32 v81, v136, v140
	v_cvt_pk_bf16_f32 v82, v130, v134
	v_cvt_pk_bf16_f32 v83, v138, v142
	v_cvt_pk_bf16_f32 v84, v129, v133
	v_cvt_pk_bf16_f32 v85, v137, v141
	v_cvt_pk_bf16_f32 v86, v131, v135
	v_cvt_pk_bf16_f32 v87, v139, v143
	v_lshl_add_u64 v[96:97], v[108:109], 0, s[36:37]
	ds_write_b128 v101, v[80:83]
	ds_write_b128 v103, v[84:87]
	v_add_co_u32_e32 v84, vcc, s70, v96
	global_load_dwordx4 v[80:83], v[96:97], off
	s_nop 0
	v_addc_co_u32_e32 v85, vcc, 0, v97, vcc
	v_add_co_u32_e32 v88, vcc, s83, v96
	global_load_dwordx4 v[84:87], v[84:85], off
	s_nop 0
	v_addc_co_u32_e32 v89, vcc, 0, v97, vcc
	v_add_co_u32_e32 v92, vcc, s3, v96
	global_load_dwordx4 v[88:91], v[88:89], off
	s_nop 0
	v_addc_co_u32_e32 v93, vcc, 0, v97, vcc
	global_load_dwordx4 v[92:95], v[92:93], off
	v_add_co_u32_e32 v96, vcc, s53, v96
	s_add_i32 s15, s15, 2
	s_nop 0
	v_addc_co_u32_e32 v97, vcc, 0, v97, vcc
	global_load_dwordx4 v[96:99], v[96:97], off
	s_cmp_gt_u32 s15, 5
	s_waitcnt lgkmcnt(0)
	s_barrier
	s_cbranch_scc0 .LBB0_1053
	s_waitcnt vmcnt(4)
	v_mov_b32_e32 v80, v145
	s_mov_b64 s[14:15], s[8:9]
	s_mov_b64 s[22:23], s[6:7]
	v_add3_u32 v144, s20, v160, v80
	s_lshl_b64 s[12:13], s[12:13], 1
	v_lshl_add_u64 v[82:83], v[144:145], 2, s[14:15]
	s_add_u32 s2, s22, s12
	s_addc_u32 s13, s23, s13
	s_add_u32 s12, s2, s19
	s_addc_u32 s13, s13, 0
	v_mov_b32_e32 v105, v145
	v_lshl_add_u64 v[80:81], s[12:13], 0, v[104:105]
	v_mov_b32_e32 v107, v145
	s_waitcnt vmcnt(0)
	v_pk_mul_f32 v[70:71], v[70:71], v[190:191] op_sel_hi:[1,0]
	v_pk_mul_f32 v[68:69], v[68:69], v[190:191] op_sel_hi:[1,0]
	v_pk_mul_f32 v[64:65], v[64:65], v[190:191] op_sel_hi:[1,0]
	v_pk_mul_f32 v[78:79], v[78:79], v[190:191] op_sel_hi:[1,0]
	v_pk_mul_f32 v[76:77], v[76:77], v[190:191] op_sel_hi:[1,0]
	v_pk_mul_f32 v[74:75], v[74:75], v[190:191] op_sel_hi:[1,0]
	v_pk_mul_f32 v[72:73], v[72:73], v[190:191] op_sel_hi:[1,0]
	v_cvt_pk_bf16_f32 v68, v68, v69
	v_cvt_pk_bf16_f32 v69, v70, v71
	v_pk_mul_f32 v[66:67], v[66:67], v[190:191] op_sel_hi:[1,0]
	v_cvt_pk_bf16_f32 v70, v64, v65
	v_lshlrev_b64 v[64:65], 12, v[144:145]
	v_cvt_pk_bf16_f32 v76, v76, v77
	v_cvt_pk_bf16_f32 v77, v78, v79
	v_cvt_pk_bf16_f32 v78, v72, v73
	v_cvt_pk_bf16_f32 v79, v74, v75
	v_cvt_pk_bf16_f32 v71, v66, v67
	v_lshl_add_u64 v[64:65], v[80:81], 0, v[64:65]
	v_permlane16_swap_b32_e32 v76, v78
	v_permlane16_swap_b32_e32 v77, v79
	v_lshl_add_u64 v[64:65], v[64:65], 0, v[106:107]
	v_permlane16_swap_b32_e32 v68, v70
	v_permlane16_swap_b32_e32 v69, v71
	global_store_dwordx4 v[64:65], v[76:79], off
	global_store_dwordx4 v[64:65], v[68:71], off offset:64
	v_add_u32_e32 v64, 16, v144
	v_mov_b32_e32 v65, v145
	v_lshl_add_u64 v[66:67], v[64:65], 2, s[14:15]
	v_pk_mul_f32 v[50:51], v[50:51], v[192:193] op_sel_hi:[1,0]
	v_pk_mul_f32 v[48:49], v[48:49], v[192:193] op_sel_hi:[1,0]
	v_pk_mul_f32 v[54:55], v[54:55], v[192:193] op_sel_hi:[1,0]
	v_cvt_pk_bf16_f32 v48, v48, v49
	v_cvt_pk_bf16_f32 v49, v50, v51
	v_pk_mul_f32 v[50:51], v[52:53], v[192:193] op_sel_hi:[1,0]
	v_pk_mul_f32 v[52:53], v[56:57], v[192:193] op_sel_hi:[1,0]
	v_cvt_pk_bf16_f32 v50, v50, v51
	v_cvt_pk_bf16_f32 v51, v54, v55
	v_pk_mul_f32 v[54:55], v[58:59], v[192:193] op_sel_hi:[1,0]
	v_cvt_pk_bf16_f32 v52, v52, v53
	v_cvt_pk_bf16_f32 v53, v54, v55
	v_pk_mul_f32 v[56:57], v[62:63], v[192:193] op_sel_hi:[1,0]
	v_pk_mul_f32 v[54:55], v[60:61], v[192:193] op_sel_hi:[1,0]
	v_permlane16_swap_b32_e32 v48, v50
	v_cvt_pk_bf16_f32 v54, v54, v55
	v_cvt_pk_bf16_f32 v55, v56, v57
	v_lshlrev_b64 v[56:57], 12, v[64:65]
	v_lshl_add_u64 v[56:57], v[80:81], 0, v[56:57]
	v_permlane16_swap_b32_e32 v49, v51
	v_lshl_add_u64 v[56:57], v[56:57], 0, v[106:107]
	global_store_dwordx4 v[56:57], v[48:51], off
	v_permlane16_swap_b32_e32 v52, v54
	v_permlane16_swap_b32_e32 v53, v55
	v_add_u32_e32 v48, 32, v144
	v_mov_b32_e32 v49, v145
	global_store_dwordx4 v[56:57], v[52:55], off offset:64
	v_lshl_add_u64 v[50:51], v[48:49], 2, s[14:15]
	v_pk_mul_f32 v[34:35], v[34:35], v[194:195] op_sel_hi:[1,0]
	v_pk_mul_f32 v[32:33], v[32:33], v[194:195] op_sel_hi:[1,0]
	v_pk_mul_f32 v[38:39], v[38:39], v[194:195] op_sel_hi:[1,0]
	v_cvt_pk_bf16_f32 v32, v32, v33
	v_cvt_pk_bf16_f32 v33, v34, v35
	v_pk_mul_f32 v[34:35], v[36:37], v[194:195] op_sel_hi:[1,0]
	v_pk_mul_f32 v[36:37], v[40:41], v[194:195] op_sel_hi:[1,0]
	v_cvt_pk_bf16_f32 v34, v34, v35
	v_cvt_pk_bf16_f32 v35, v38, v39
	v_pk_mul_f32 v[38:39], v[42:43], v[194:195] op_sel_hi:[1,0]
	v_cvt_pk_bf16_f32 v36, v36, v37
	v_cvt_pk_bf16_f32 v37, v38, v39
	v_pk_mul_f32 v[40:41], v[46:47], v[194:195] op_sel_hi:[1,0]
	v_pk_mul_f32 v[38:39], v[44:45], v[194:195] op_sel_hi:[1,0]
	v_permlane16_swap_b32_e32 v32, v34
	v_cvt_pk_bf16_f32 v38, v38, v39
	v_cvt_pk_bf16_f32 v39, v40, v41
	v_lshlrev_b64 v[40:41], 12, v[48:49]
	v_lshl_add_u64 v[40:41], v[80:81], 0, v[40:41]
	v_permlane16_swap_b32_e32 v33, v35
	v_lshl_add_u64 v[40:41], v[40:41], 0, v[106:107]
	global_store_dwordx4 v[40:41], v[32:35], off
	v_permlane16_swap_b32_e32 v36, v38
	v_permlane16_swap_b32_e32 v37, v39
	v_add_u32_e32 v32, 48, v144
	v_mov_b32_e32 v33, v145
	global_store_dwordx4 v[40:41], v[36:39], off offset:64
	v_lshl_add_u64 v[34:35], v[32:33], 2, s[14:15]
	v_add_u32_e32 v144, 64, v144
	v_pk_mul_f32 v[18:19], v[18:19], v[196:197] op_sel_hi:[1,0]
	v_pk_mul_f32 v[16:17], v[16:17], v[196:197] op_sel_hi:[1,0]
	v_pk_mul_f32 v[22:23], v[22:23], v[196:197] op_sel_hi:[1,0]
	v_cvt_pk_bf16_f32 v16, v16, v17
	v_cvt_pk_bf16_f32 v17, v18, v19
	v_pk_mul_f32 v[18:19], v[20:21], v[196:197] op_sel_hi:[1,0]
	v_pk_mul_f32 v[20:21], v[24:25], v[196:197] op_sel_hi:[1,0]
	v_cvt_pk_bf16_f32 v18, v18, v19
	v_cvt_pk_bf16_f32 v19, v22, v23
	v_pk_mul_f32 v[22:23], v[26:27], v[196:197] op_sel_hi:[1,0]
	v_cvt_pk_bf16_f32 v20, v20, v21
	v_cvt_pk_bf16_f32 v21, v22, v23
	v_pk_mul_f32 v[24:25], v[30:31], v[196:197] op_sel_hi:[1,0]
	v_pk_mul_f32 v[22:23], v[28:29], v[196:197] op_sel_hi:[1,0]
	v_permlane16_swap_b32_e32 v16, v18
	v_cvt_pk_bf16_f32 v22, v22, v23
	v_cvt_pk_bf16_f32 v23, v24, v25
	v_lshlrev_b64 v[24:25], 12, v[32:33]
	v_lshl_add_u64 v[24:25], v[80:81], 0, v[24:25]
	v_permlane16_swap_b32_e32 v17, v19
	v_lshl_add_u64 v[24:25], v[24:25], 0, v[106:107]
	v_permlane16_swap_b32_e32 v20, v22
	v_permlane16_swap_b32_e32 v21, v23
	global_store_dwordx4 v[24:25], v[16:19], off
	global_store_dwordx4 v[24:25], v[20:23], off offset:64
	s_nop 0
	v_lshl_add_u64 v[16:17], v[144:145], 2, s[14:15]
	v_pk_mul_f32 v[2:3], v[2:3], v[198:199] op_sel_hi:[1,0]
	v_pk_mul_f32 v[0:1], v[0:1], v[198:199] op_sel_hi:[1,0]
	v_pk_mul_f32 v[6:7], v[6:7], v[198:199] op_sel_hi:[1,0]
	v_cvt_pk_bf16_f32 v0, v0, v1
	v_cvt_pk_bf16_f32 v1, v2, v3
	v_pk_mul_f32 v[2:3], v[4:5], v[198:199] op_sel_hi:[1,0]
	v_pk_mul_f32 v[4:5], v[8:9], v[198:199] op_sel_hi:[1,0]
	v_cvt_pk_bf16_f32 v2, v2, v3
	v_cvt_pk_bf16_f32 v3, v6, v7
	v_pk_mul_f32 v[6:7], v[10:11], v[198:199] op_sel_hi:[1,0]
	v_cvt_pk_bf16_f32 v4, v4, v5
	v_cvt_pk_bf16_f32 v5, v6, v7
	v_pk_mul_f32 v[8:9], v[14:15], v[198:199] op_sel_hi:[1,0]
	v_pk_mul_f32 v[6:7], v[12:13], v[198:199] op_sel_hi:[1,0]
	v_permlane16_swap_b32_e32 v0, v2
	v_cvt_pk_bf16_f32 v6, v6, v7
	v_cvt_pk_bf16_f32 v7, v8, v9
	v_lshlrev_b64 v[8:9], 12, v[144:145]
	v_lshl_add_u64 v[8:9], v[80:81], 0, v[8:9]
	v_permlane16_swap_b32_e32 v1, v3
	v_lshl_add_u64 v[8:9], v[8:9], 0, v[106:107]
	v_permlane16_swap_b32_e32 v4, v6
	v_permlane16_swap_b32_e32 v5, v7
	global_store_dwordx4 v[8:9], v[0:3], off
	global_store_dwordx4 v[8:9], v[4:7], off offset:64
	s_branch .LBB0_1050

.LBB0_1101:
	s_or_b64 exec, exec, s[4:5]
	s_add_u32 s4, s2, 0x3600
	s_addc_u32 s5, s1, 0
	s_add_u32 s10, s7, 0x29b9fd00
	s_addc_u32 s11, s6, 0
	s_ashr_i32 s1, s0, 31
	s_lshl_b64 s[0:1], s[0:1], 13
	s_add_u32 s6, s9, s0
	v_lshlrev_b32_e32 v144, 4, v32
	s_addc_u32 s7, s8, s1
	v_or_b32_e32 v72, 0x1000, v144
	v_or_b32_e32 v70, 0x1400, v144
	v_or_b32_e32 v68, 0x1800, v144
	v_or_b32_e32 v66, 0x1c00, v144
	s_add_u32 s0, s13, 0x4ab9fd00
	global_load_dwordx4 v[28:31], v144, s[6:7]
	global_load_dwordx4 v[24:27], v144, s[6:7] offset:1024
	global_load_dwordx4 v[20:23], v144, s[6:7] offset:2048
	global_load_dwordx4 v[16:19], v144, s[6:7] offset:3072
	global_load_dwordx4 v[12:15], v72, s[6:7]
	global_load_dwordx4 v[8:11], v70, s[6:7]
	global_load_dwordx4 v[4:7], v68, s[6:7]
	global_load_dwordx4 v[0:3], v66, s[6:7]
	s_waitcnt vmcnt(0) lgkmcnt(0)
	v_lshlrev_b32_e32 v64, 3, v32
	v_mov_b32_e32 v65, 0
	v_mov_b32_e32 v67, 0
	v_lshlrev_b32_e32 v96, 2, v32
	s_add_u32 s14, s13, 0x4ab9fd00
	s_addc_u32 s15, s12, 0
	s_mov_b32 s16, 0
.Lcombine_token:
	s_lshl_b32 s17, s16, 1
	s_nop 3
	v_readlane_b32 s18, v106, s17
	s_add_u32 s17, s17, 1
	s_nop 3
	v_readlane_b32 s19, v106, s17
	s_lshl_b32 s20, s16, 11
	v_add_u32_e32 v66, s20, v74
	v_lshlrev_b64 v[68:69], 13, v[66:67]
	v_lshl_add_u64 v[70:71], s[4:5], 0, v[68:69]
	v_lshl_add_u64 v[70:71], v[70:71], 0, v[144:145]
	v_add_co_u32_e32 v76, vcc, 0x1000, v70
	s_nop 1
	v_addc_co_u32_e32 v77, vcc, 0, v71, vcc
	v_lshlrev_b64 v[68:69], 12, v[66:67]
	v_lshl_add_u64 v[72:73], s[14:15], 0, v[68:69]
	v_lshl_add_u64 v[72:73], v[72:73], 0, v[64:65]
	s_lshl_b32 s21, s18, 12
	s_add_u32 s22, s10, s21
	s_addc_u32 s23, s11, 0
	s_lshl_b32 s21, s19, 12
	s_add_u32 s24, s10, s21
	s_addc_u32 s25, s11, 0
	s_nop 4
	global_load_dwordx4 v[32:35], v[70:71], off
	global_load_dwordx2 v[146:147], v64, s[22:23]
	global_load_dwordx2 v[162:163], v64, s[24:25]
	global_load_dwordx4 v[36:39], v[70:71], off offset:1024
	global_load_dwordx2 v[148:149], v64, s[22:23] offset:512
	global_load_dwordx2 v[164:165], v64, s[24:25] offset:512
	global_load_dwordx4 v[40:43], v[70:71], off offset:2048
	global_load_dwordx2 v[150:151], v64, s[22:23] offset:1024
	global_load_dwordx2 v[166:167], v64, s[24:25] offset:1024
	global_load_dwordx4 v[44:47], v[70:71], off offset:3072
	global_load_dwordx2 v[152:153], v64, s[22:23] offset:1536
	global_load_dwordx2 v[168:169], v64, s[24:25] offset:1536
	global_load_dwordx4 v[48:51], v[76:77], off
	global_load_dwordx2 v[154:155], v64, s[22:23] offset:2048
	global_load_dwordx2 v[170:171], v64, s[24:25] offset:2048
	global_load_dwordx4 v[52:55], v[76:77], off offset:1024
	global_load_dwordx2 v[156:157], v64, s[22:23] offset:2560
	global_load_dwordx2 v[172:173], v64, s[24:25] offset:2560
	global_load_dwordx4 v[56:59], v[76:77], off offset:2048
	global_load_dwordx2 v[158:159], v64, s[22:23] offset:3072
	global_load_dwordx2 v[174:175], v64, s[24:25] offset:3072
	global_load_dwordx4 v[60:63], v[76:77], off offset:3072
	global_load_dwordx2 v[160:161], v64, s[22:23] offset:3584
	global_load_dwordx2 v[176:177], v64, s[24:25] offset:3584
	s_waitcnt vmcnt(21)
	v_lshlrev_b32_e32 v80, 16, v146
	v_and_b32_e32 v81, 0xffff0000, v146
	v_lshlrev_b32_e32 v82, 16, v162
	v_and_b32_e32 v83, 0xffff0000, v162
	v_lshlrev_b32_e32 v84, 16, v147
	v_and_b32_e32 v85, 0xffff0000, v147
	v_lshlrev_b32_e32 v86, 16, v163
	v_and_b32_e32 v87, 0xffff0000, v163
	v_pk_add_f32 v[80:81], v[80:81], v[82:83]
	v_pk_add_f32 v[84:85], v[84:85], v[86:87]
	v_pk_add_f32 v[32:33], v[32:33], v[80:81]
	v_pk_add_f32 v[34:35], v[34:35], v[84:85]
	global_store_dwordx4 v[70:71], v[32:35], off
	v_pk_mul_f32 v[80:81], v[32:33], v[32:33]
	v_pk_mul_f32 v[82:83], v[34:35], v[34:35]
	v_add_f32_e32 v80, v80, v81
	v_add_f32_e32 v80, v82, v80
	v_add_f32_e32 v80, v83, v80
	v_mov_b32_e32 v90, v80
	s_waitcnt vmcnt(19)
	v_lshlrev_b32_e32 v80, 16, v148
	v_and_b32_e32 v81, 0xffff0000, v148
	v_lshlrev_b32_e32 v82, 16, v164
	v_and_b32_e32 v83, 0xffff0000, v164
	v_lshlrev_b32_e32 v84, 16, v149
	v_and_b32_e32 v85, 0xffff0000, v149
	v_lshlrev_b32_e32 v86, 16, v165
	v_and_b32_e32 v87, 0xffff0000, v165
	v_pk_add_f32 v[80:81], v[80:81], v[82:83]
	v_pk_add_f32 v[84:85], v[84:85], v[86:87]
	v_pk_add_f32 v[36:37], v[36:37], v[80:81]
	v_pk_add_f32 v[38:39], v[38:39], v[84:85]
	global_store_dwordx4 v[70:71], v[36:39], off offset:1024
	v_pk_mul_f32 v[80:81], v[36:37], v[36:37]
	v_pk_mul_f32 v[82:83], v[38:39], v[38:39]
	v_add_f32_e32 v80, v80, v81
	v_add_f32_e32 v80, v82, v80
	v_add_f32_e32 v80, v83, v80
	v_add_f32_e32 v90, v90, v80
	s_waitcnt vmcnt(17)
	v_lshlrev_b32_e32 v80, 16, v150
	v_and_b32_e32 v81, 0xffff0000, v150
	v_lshlrev_b32_e32 v82, 16, v166
	v_and_b32_e32 v83, 0xffff0000, v166
	v_lshlrev_b32_e32 v84, 16, v151
	v_and_b32_e32 v85, 0xffff0000, v151
	v_lshlrev_b32_e32 v86, 16, v167
	v_and_b32_e32 v87, 0xffff0000, v167
	v_pk_add_f32 v[80:81], v[80:81], v[82:83]
	v_pk_add_f32 v[84:85], v[84:85], v[86:87]
	v_pk_add_f32 v[40:41], v[40:41], v[80:81]
	v_pk_add_f32 v[42:43], v[42:43], v[84:85]
	global_store_dwordx4 v[70:71], v[40:43], off offset:2048
	v_pk_mul_f32 v[80:81], v[40:41], v[40:41]
	v_pk_mul_f32 v[82:83], v[42:43], v[42:43]
	v_add_f32_e32 v80, v80, v81
	v_add_f32_e32 v80, v82, v80
	v_add_f32_e32 v80, v83, v80
	v_add_f32_e32 v90, v90, v80
	s_waitcnt vmcnt(15)
	v_lshlrev_b32_e32 v80, 16, v152
	v_and_b32_e32 v81, 0xffff0000, v152
	v_lshlrev_b32_e32 v82, 16, v168
	v_and_b32_e32 v83, 0xffff0000, v168
	v_lshlrev_b32_e32 v84, 16, v153
	v_and_b32_e32 v85, 0xffff0000, v153
	v_lshlrev_b32_e32 v86, 16, v169
	v_and_b32_e32 v87, 0xffff0000, v169
	v_pk_add_f32 v[80:81], v[80:81], v[82:83]
	v_pk_add_f32 v[84:85], v[84:85], v[86:87]
	v_pk_add_f32 v[44:45], v[44:45], v[80:81]
	v_pk_add_f32 v[46:47], v[46:47], v[84:85]
	global_store_dwordx4 v[70:71], v[44:47], off offset:3072
	v_pk_mul_f32 v[80:81], v[44:45], v[44:45]
	v_pk_mul_f32 v[82:83], v[46:47], v[46:47]
	v_add_f32_e32 v80, v80, v81
	v_add_f32_e32 v80, v82, v80
	v_add_f32_e32 v80, v83, v80
	v_add_f32_e32 v90, v90, v80
	s_waitcnt vmcnt(13)
	v_lshlrev_b32_e32 v80, 16, v154
	v_and_b32_e32 v81, 0xffff0000, v154
	v_lshlrev_b32_e32 v82, 16, v170
	v_and_b32_e32 v83, 0xffff0000, v170
	v_lshlrev_b32_e32 v84, 16, v155
	v_and_b32_e32 v85, 0xffff0000, v155
	v_lshlrev_b32_e32 v86, 16, v171
	v_and_b32_e32 v87, 0xffff0000, v171
	v_pk_add_f32 v[80:81], v[80:81], v[82:83]
	v_pk_add_f32 v[84:85], v[84:85], v[86:87]
	v_pk_add_f32 v[48:49], v[48:49], v[80:81]
	v_pk_add_f32 v[50:51], v[50:51], v[84:85]
	global_store_dwordx4 v[76:77], v[48:51], off
	v_pk_mul_f32 v[80:81], v[48:49], v[48:49]
	v_pk_mul_f32 v[82:83], v[50:51], v[50:51]
	v_add_f32_e32 v80, v80, v81
	v_add_f32_e32 v80, v82, v80
	v_add_f32_e32 v80, v83, v80
	v_add_f32_e32 v90, v90, v80
	s_waitcnt vmcnt(11)
	v_lshlrev_b32_e32 v80, 16, v156
	v_and_b32_e32 v81, 0xffff0000, v156
	v_lshlrev_b32_e32 v82, 16, v172
	v_and_b32_e32 v83, 0xffff0000, v172
	v_lshlrev_b32_e32 v84, 16, v157
	v_and_b32_e32 v85, 0xffff0000, v157
	v_lshlrev_b32_e32 v86, 16, v173
	v_and_b32_e32 v87, 0xffff0000, v173
	v_pk_add_f32 v[80:81], v[80:81], v[82:83]
	v_pk_add_f32 v[84:85], v[84:85], v[86:87]
	v_pk_add_f32 v[52:53], v[52:53], v[80:81]
	v_pk_add_f32 v[54:55], v[54:55], v[84:85]
	global_store_dwordx4 v[76:77], v[52:55], off offset:1024
	v_pk_mul_f32 v[80:81], v[52:53], v[52:53]
	v_pk_mul_f32 v[82:83], v[54:55], v[54:55]
	v_add_f32_e32 v80, v80, v81
	v_add_f32_e32 v80, v82, v80
	v_add_f32_e32 v80, v83, v80
	v_add_f32_e32 v90, v90, v80
	s_waitcnt vmcnt(9)
	v_lshlrev_b32_e32 v80, 16, v158
	v_and_b32_e32 v81, 0xffff0000, v158
	v_lshlrev_b32_e32 v82, 16, v174
	v_and_b32_e32 v83, 0xffff0000, v174
	v_lshlrev_b32_e32 v84, 16, v159
	v_and_b32_e32 v85, 0xffff0000, v159
	v_lshlrev_b32_e32 v86, 16, v175
	v_and_b32_e32 v87, 0xffff0000, v175
	v_pk_add_f32 v[80:81], v[80:81], v[82:83]
	v_pk_add_f32 v[84:85], v[84:85], v[86:87]
	v_pk_add_f32 v[56:57], v[56:57], v[80:81]
	v_pk_add_f32 v[58:59], v[58:59], v[84:85]
	global_store_dwordx4 v[76:77], v[56:59], off offset:2048
	v_pk_mul_f32 v[80:81], v[56:57], v[56:57]
	v_pk_mul_f32 v[82:83], v[58:59], v[58:59]
	v_add_f32_e32 v80, v80, v81
	v_add_f32_e32 v80, v82, v80
	v_add_f32_e32 v80, v83, v80
	v_add_f32_e32 v90, v90, v80
	s_waitcnt vmcnt(7)
	v_lshlrev_b32_e32 v80, 16, v160
	v_and_b32_e32 v81, 0xffff0000, v160
	v_lshlrev_b32_e32 v82, 16, v176
	v_and_b32_e32 v83, 0xffff0000, v176
	v_lshlrev_b32_e32 v84, 16, v161
	v_and_b32_e32 v85, 0xffff0000, v161
	v_lshlrev_b32_e32 v86, 16, v177
	v_and_b32_e32 v87, 0xffff0000, v177
	v_pk_add_f32 v[80:81], v[80:81], v[82:83]
	v_pk_add_f32 v[84:85], v[84:85], v[86:87]
	v_pk_add_f32 v[60:61], v[60:61], v[80:81]
	v_pk_add_f32 v[62:63], v[62:63], v[84:85]
	global_store_dwordx4 v[76:77], v[60:63], off offset:3072
	v_pk_mul_f32 v[80:81], v[60:61], v[60:61]
	v_pk_mul_f32 v[82:83], v[62:63], v[62:63]
	v_add_f32_e32 v80, v80, v81
	v_add_f32_e32 v80, v82, v80
	v_add_f32_e32 v80, v83, v80
	v_add_f32_e32 v90, v90, v80
	v_xor_b32_e32 v92, 128, v96
	ds_bpermute_b32 v91, v92, v90
	s_waitcnt lgkmcnt(0)
	v_add_f32_e32 v90, v90, v91
	v_xor_b32_e32 v92, 64, v96
	ds_bpermute_b32 v91, v92, v90
	s_waitcnt lgkmcnt(0)
	v_add_f32_e32 v90, v90, v91
	v_xor_b32_e32 v92, 32, v96
	ds_bpermute_b32 v91, v92, v90
	s_waitcnt lgkmcnt(0)
	v_add_f32_e32 v90, v90, v91
	v_xor_b32_e32 v92, 16, v96
	ds_bpermute_b32 v91, v92, v90
	s_waitcnt lgkmcnt(0)
	v_add_f32_e32 v90, v90, v91
	v_xor_b32_e32 v92, 8, v96
	ds_bpermute_b32 v91, v92, v90
	s_waitcnt lgkmcnt(0)
	v_add_f32_e32 v90, v90, v91
	v_xor_b32_e32 v92, 4, v96
	ds_bpermute_b32 v91, v92, v90
	s_waitcnt lgkmcnt(0)
	v_add_f32_e32 v90, v90, v91
	v_fmamk_f32 v90, v90, 0x3a000000, v204
	v_rsq_f32_e32 v90, v90
	s_nop 0
	v_pk_mul_f32 v[80:81], v[32:33], v[90:91] op_sel_hi:[1,0]
	v_pk_mul_f32 v[82:83], v[34:35], v[90:91] op_sel_hi:[1,0]
	v_pk_mul_f32 v[80:81], v[28:29], v[80:81]
	v_pk_mul_f32 v[82:83], v[30:31], v[82:83]
	v_cvt_pk_bf16_f32 v84, v80, v81
	v_cvt_pk_bf16_f32 v85, v82, v83
	global_store_dwordx2 v[72:73], v[84:85], off
	v_pk_mul_f32 v[80:81], v[36:37], v[90:91] op_sel_hi:[1,0]
	v_pk_mul_f32 v[82:83], v[38:39], v[90:91] op_sel_hi:[1,0]
	v_pk_mul_f32 v[80:81], v[24:25], v[80:81]
	v_pk_mul_f32 v[82:83], v[26:27], v[82:83]
	v_cvt_pk_bf16_f32 v84, v80, v81
	v_cvt_pk_bf16_f32 v85, v82, v83
	global_store_dwordx2 v[72:73], v[84:85], off offset:512
	v_pk_mul_f32 v[80:81], v[40:41], v[90:91] op_sel_hi:[1,0]
	v_pk_mul_f32 v[82:83], v[42:43], v[90:91] op_sel_hi:[1,0]
	v_pk_mul_f32 v[80:81], v[20:21], v[80:81]
	v_pk_mul_f32 v[82:83], v[22:23], v[82:83]
	v_cvt_pk_bf16_f32 v84, v80, v81
	v_cvt_pk_bf16_f32 v85, v82, v83
	global_store_dwordx2 v[72:73], v[84:85], off offset:1024
	v_pk_mul_f32 v[80:81], v[44:45], v[90:91] op_sel_hi:[1,0]
	v_pk_mul_f32 v[82:83], v[46:47], v[90:91] op_sel_hi:[1,0]
	v_pk_mul_f32 v[80:81], v[16:17], v[80:81]
	v_pk_mul_f32 v[82:83], v[18:19], v[82:83]
	v_cvt_pk_bf16_f32 v84, v80, v81
	v_cvt_pk_bf16_f32 v85, v82, v83
	global_store_dwordx2 v[72:73], v[84:85], off offset:1536
	v_pk_mul_f32 v[80:81], v[48:49], v[90:91] op_sel_hi:[1,0]
	v_pk_mul_f32 v[82:83], v[50:51], v[90:91] op_sel_hi:[1,0]
	v_pk_mul_f32 v[80:81], v[12:13], v[80:81]
	v_pk_mul_f32 v[82:83], v[14:15], v[82:83]
	v_cvt_pk_bf16_f32 v84, v80, v81
	v_cvt_pk_bf16_f32 v85, v82, v83
	global_store_dwordx2 v[72:73], v[84:85], off offset:2048
	v_pk_mul_f32 v[80:81], v[52:53], v[90:91] op_sel_hi:[1,0]
	v_pk_mul_f32 v[82:83], v[54:55], v[90:91] op_sel_hi:[1,0]
	v_pk_mul_f32 v[80:81], v[8:9], v[80:81]
	v_pk_mul_f32 v[82:83], v[10:11], v[82:83]
	v_cvt_pk_bf16_f32 v84, v80, v81
	v_cvt_pk_bf16_f32 v85, v82, v83
	global_store_dwordx2 v[72:73], v[84:85], off offset:2560
	v_pk_mul_f32 v[80:81], v[56:57], v[90:91] op_sel_hi:[1,0]
	v_pk_mul_f32 v[82:83], v[58:59], v[90:91] op_sel_hi:[1,0]
	v_pk_mul_f32 v[80:81], v[4:5], v[80:81]
	v_pk_mul_f32 v[82:83], v[6:7], v[82:83]
	v_cvt_pk_bf16_f32 v84, v80, v81
	v_cvt_pk_bf16_f32 v85, v82, v83
	global_store_dwordx2 v[72:73], v[84:85], off offset:3072
	v_pk_mul_f32 v[80:81], v[60:61], v[90:91] op_sel_hi:[1,0]
	v_pk_mul_f32 v[82:83], v[62:63], v[90:91] op_sel_hi:[1,0]
	v_pk_mul_f32 v[80:81], v[0:1], v[80:81]
	v_pk_mul_f32 v[82:83], v[2:3], v[82:83]
	v_cvt_pk_bf16_f32 v84, v80, v81
	v_cvt_pk_bf16_f32 v85, v82, v83
	global_store_dwordx2 v[72:73], v[84:85], off offset:3584
	s_add_u32 s16, s16, 1
	s_cmp_lt_u32 s16, 4
	s_cbranch_scc1 .Lcombine_token
	v_readlane_b32 s34, v254, 4
	s_mov_b32 s0, s37
	s_mov_b32 s1, s33
	s_nop 0
	v_mbcnt_lo_u32_b32 v0, -1, s0
	v_mbcnt_hi_u32_b32 v0, -1, v0
	v_lshl_or_b32 v2, s1, 6, v0
	v_readlane_b32 s0, v254, 0
	s_mov_b32 s0, s37
	s_add_i32 s0, s0, 0x20120
	v_mov_b32_e32 v0, s0
	ds_read_b64 v[0:1], v0
	s_waitcnt vmcnt(0)
	v_cmp_eq_u32_e32 vcc, 0, v2
	v_readlane_b32 s1, v254, 1
	s_waitcnt lgkmcnt(0)
	v_readfirstlane_b32 s63, v1
	v_readfirstlane_b32 s62, v0
	s_barrier
	s_and_saveexec_b64 s[64:65], vcc
	s_cbranch_execz .LBB0_1145
	v_mov_b32_e32 v0, s67
	s_waitcnt vmcnt(0) expcnt(0) lgkmcnt(0)
	ds_read_b32 v2, v0
	v_mov_b32_e32 v0, s68
	ds_read_b32 v0, v0
	s_waitcnt lgkmcnt(1)
	v_cmp_ne_u32_e32 vcc, 0, v2
	s_cbranch_vccnz .LBB0_1116
	v_readlane_b32 s0, v254, 5
	v_readlane_b32 s1, v254, 6
	s_load_dwordx2 s[6:7], s[0:1], 0x0
	s_load_dword s2, s[0:1], 0x8
	s_add_u32 s0, s62, 0x1000
	s_addc_u32 s1, s63, 0
	s_add_u32 s4, s62, 0x1100
	s_waitcnt lgkmcnt(0)
	s_mul_i32 s5, s7, s6
	s_mul_i32 s2, s5, s2
	s_addc_u32 s5, s63, 0
	s_add_u32 s6, s62, 0x1200
	s_addc_u32 s7, s63, 0
	s_add_u32 s8, s62, 0x1300
	s_addc_u32 s9, s63, 0
	s_mov_b32 s28, 1
	s_mov_b64 s[10:11], 0
	s_branch .LBB0_1106
